# v8: GEMM unit boundaries - one extra barrier per 4-wave group (group 0 before, group 1 after the epilogue) so both groups run their epilogues at the same time instead of one after the other
# speedup vs baseline: 1.0132x; 1.0071x over previous
.LBB0_215:
	ds_read_b128 v[10:13], v175
	ds_read_b128 v[14:17], v175 offset:1024
	ds_read_b128 v[166:169], v175 offset:2048
	ds_read_b128 v[170:173], v175 offset:3072
	s_add_u32 s28, s8, 0xfffc0080
	s_addc_u32 s29, s9, -1
	s_cmp_eq_u32 s64, 12
	s_cselect_b32 s31, s13, s29
	s_cselect_b32 s30, s21, s28
	s_cselect_b32 s29, s15, s63
	s_cselect_b32 s28, s51, s62
	s_mov_b32 m0, s52
	v_lshl_add_u64 v[2:3], s[8:9], 0, v[158:159]
	ds_read_b128 v[180:183], v176
	ds_read_b128 v[184:187], v176 offset:1024
	ds_read_b128 v[188:191], v176 offset:2048
	ds_read_b128 v[192:195], v176 offset:3072
	ds_read_b128 v[196:199], v176 offset:4096
	ds_read_b128 v[200:203], v176 offset:5120
	ds_read_b128 v[204:207], v176 offset:6144
	ds_read_b128 v[208:211], v176 offset:7168
	global_load_lds_dwordx4 v[2:3], off
	v_lshl_add_u64 v[2:3], s[8:9], 0, v[160:161]
	s_mov_b32 m0, s53
	s_nop 0
	global_load_lds_dwordx4 v[2:3], off
	ds_read_b128 v[212:215], v177
	ds_read_b128 v[216:219], v177 offset:1024
	ds_read_b128 v[220:223], v177 offset:2048
	ds_read_b128 v[224:227], v177 offset:3072
	s_waitcnt vmcnt(8) lgkmcnt(0)
	s_barrier
	s_setprio 1
	v_mfma_f32_16x16x128_f8f6f4 v[138:141], v[10:17], v[180:187], v[138:141]
	v_mfma_f32_16x16x128_f8f6f4 v[134:137], v[166:173], v[180:187], v[134:137]
	v_mfma_f32_16x16x128_f8f6f4 v[122:125], v[10:17], v[188:195], v[122:125]
	v_mfma_f32_16x16x128_f8f6f4 v[118:121], v[166:173], v[188:195], v[118:121]
	v_mfma_f32_16x16x128_f8f6f4 v[98:101], v[10:17], v[196:203], v[98:101]
	v_mfma_f32_16x16x128_f8f6f4 v[90:93], v[166:173], v[196:203], v[90:93]
	v_mfma_f32_16x16x128_f8f6f4 v[70:73], v[10:17], v[204:211], v[70:73]
	v_mfma_f32_16x16x128_f8f6f4 v[58:61], v[166:173], v[204:211], v[58:61]
	v_mfma_f32_16x16x128_f8f6f4 v[146:149], v[212:219], v[180:187], v[146:149]
	v_mfma_f32_16x16x128_f8f6f4 v[142:145], v[220:227], v[180:187], v[142:145]
	v_mfma_f32_16x16x128_f8f6f4 v[130:133], v[212:219], v[188:195], v[130:133]
	v_mfma_f32_16x16x128_f8f6f4 v[126:129], v[220:227], v[188:195], v[126:129]
	v_mfma_f32_16x16x128_f8f6f4 v[114:117], v[212:219], v[196:203], v[114:117]
	v_mfma_f32_16x16x128_f8f6f4 v[110:113], v[220:227], v[196:203], v[110:113]
	v_mfma_f32_16x16x128_f8f6f4 v[82:85], v[212:219], v[204:211], v[82:85]
	v_mfma_f32_16x16x128_f8f6f4 v[78:81], v[220:227], v[204:211], v[78:81]
	s_setprio 0
	s_barrier
	ds_read_b128 v[180:183], v176 offset:16384
	ds_read_b128 v[184:187], v176 offset:17408
	ds_read_b128 v[188:191], v176 offset:18432
	ds_read_b128 v[192:195], v176 offset:19456
	ds_read_b128 v[196:199], v176 offset:20480
	ds_read_b128 v[200:203], v176 offset:21504
	ds_read_b128 v[204:207], v176 offset:22528
	ds_read_b128 v[208:211], v176 offset:23552
	s_mov_b32 m0, s54
	v_lshl_add_u64 v[6:7], s[28:29], 0, v[154:155]
	global_load_lds_dwordx4 v[6:7], off
	v_lshl_add_u64 v[8:9], s[28:29], 0, v[150:151]
	s_mov_b32 m0, s55
	s_nop 0
	global_load_lds_dwordx4 v[8:9], off
	s_mov_b32 m0, s27
	v_lshl_add_u64 v[2:3], s[30:31], 0, v[156:157]
	global_load_lds_dwordx4 v[2:3], off
	v_lshl_add_u64 v[4:5], s[30:31], 0, v[152:153]
	s_mov_b32 m0, s41
	s_nop 0
	global_load_lds_dwordx4 v[4:5], off
	s_add_u32 s66, s28, 0x40000
	s_addc_u32 s67, s29, 0
	s_mov_b32 m0, s56
	v_lshl_add_u64 v[228:229], s[66:67], 0, v[154:155]
	global_load_lds_dwordx4 v[228:229], off
	v_lshl_add_u64 v[228:229], s[66:67], 0, v[150:151]
	s_mov_b32 m0, s57
	s_nop 0
	global_load_lds_dwordx4 v[228:229], off
	s_waitcnt vmcnt(8) lgkmcnt(0)
	s_barrier
	s_setprio 1
	v_mfma_f32_16x16x128_f8f6f4 v[94:97], v[10:17], v[180:187], v[94:97]
	v_mfma_f32_16x16x128_f8f6f4 v[86:89], v[166:173], v[180:187], v[86:89]
	v_mfma_f32_16x16x128_f8f6f4 v[66:69], v[10:17], v[188:195], v[66:69]
	v_mfma_f32_16x16x128_f8f6f4 v[54:57], v[166:173], v[188:195], v[54:57]
	v_mfma_f32_16x16x128_f8f6f4 v[46:49], v[10:17], v[196:203], v[46:49]
	v_mfma_f32_16x16x128_f8f6f4 v[38:41], v[166:173], v[196:203], v[38:41]
	v_mfma_f32_16x16x128_f8f6f4 v[30:33], v[10:17], v[204:211], v[30:33]
	v_mfma_f32_16x16x128_f8f6f4 v[22:25], v[166:173], v[204:211], v[22:25]
	v_mfma_f32_16x16x128_f8f6f4 v[106:109], v[212:219], v[180:187], v[106:109]
	v_mfma_f32_16x16x128_f8f6f4 v[102:105], v[220:227], v[180:187], v[102:105]
	v_mfma_f32_16x16x128_f8f6f4 v[74:77], v[212:219], v[188:195], v[74:77]
	v_mfma_f32_16x16x128_f8f6f4 v[62:65], v[220:227], v[188:195], v[62:65]
	v_mfma_f32_16x16x128_f8f6f4 v[50:53], v[212:219], v[196:203], v[50:53]
	v_mfma_f32_16x16x128_f8f6f4 v[42:45], v[220:227], v[196:203], v[42:45]
	v_mfma_f32_16x16x128_f8f6f4 v[34:37], v[212:219], v[204:211], v[34:37]
	v_mfma_f32_16x16x128_f8f6f4 v[26:29], v[220:227], v[204:211], v[26:29]
	s_setprio 0
	s_barrier
	ds_read_b128 v[10:13], v178
	ds_read_b128 v[14:17], v178 offset:1024
	ds_read_b128 v[166:169], v178 offset:2048
	ds_read_b128 v[170:173], v178 offset:3072
	s_add_u32 s30, s30, 0x40000
	s_addc_u32 s31, s31, 0
	s_mov_b32 m0, s42
	v_lshl_add_u64 v[212:213], s[30:31], 0, v[156:157]
	ds_read_b128 v[180:183], v176 offset:32768
	ds_read_b128 v[184:187], v176 offset:33792
	ds_read_b128 v[188:191], v176 offset:34816
	ds_read_b128 v[192:195], v176 offset:35840
	ds_read_b128 v[196:199], v176 offset:36864
	ds_read_b128 v[200:203], v176 offset:37888
	ds_read_b128 v[204:207], v176 offset:38912
	ds_read_b128 v[208:211], v176 offset:39936
	global_load_lds_dwordx4 v[212:213], off
	v_lshl_add_u64 v[212:213], s[30:31], 0, v[152:153]
	s_mov_b32 m0, s43
	s_nop 0
	global_load_lds_dwordx4 v[212:213], off
	ds_read_b128 v[212:215], v179
	ds_read_b128 v[216:219], v179 offset:1024
	ds_read_b128 v[220:223], v179 offset:2048
	ds_read_b128 v[224:227], v179 offset:3072
	s_waitcnt vmcnt(8) lgkmcnt(0)
	s_barrier
	s_setprio 1
	v_mfma_f32_16x16x128_f8f6f4 v[138:141], v[10:17], v[180:187], v[138:141]
	v_mfma_f32_16x16x128_f8f6f4 v[134:137], v[166:173], v[180:187], v[134:137]
	v_mfma_f32_16x16x128_f8f6f4 v[122:125], v[10:17], v[188:195], v[122:125]
	v_mfma_f32_16x16x128_f8f6f4 v[118:121], v[166:173], v[188:195], v[118:121]
	v_mfma_f32_16x16x128_f8f6f4 v[98:101], v[10:17], v[196:203], v[98:101]
	v_mfma_f32_16x16x128_f8f6f4 v[90:93], v[166:173], v[196:203], v[90:93]
	v_mfma_f32_16x16x128_f8f6f4 v[70:73], v[10:17], v[204:211], v[70:73]
	v_mfma_f32_16x16x128_f8f6f4 v[58:61], v[166:173], v[204:211], v[58:61]
	v_mfma_f32_16x16x128_f8f6f4 v[146:149], v[212:219], v[180:187], v[146:149]
	v_mfma_f32_16x16x128_f8f6f4 v[142:145], v[220:227], v[180:187], v[142:145]
	v_mfma_f32_16x16x128_f8f6f4 v[130:133], v[212:219], v[188:195], v[130:133]
	v_mfma_f32_16x16x128_f8f6f4 v[126:129], v[220:227], v[188:195], v[126:129]
	v_mfma_f32_16x16x128_f8f6f4 v[114:117], v[212:219], v[196:203], v[114:117]
	v_mfma_f32_16x16x128_f8f6f4 v[110:113], v[220:227], v[196:203], v[110:113]
	v_mfma_f32_16x16x128_f8f6f4 v[82:85], v[212:219], v[204:211], v[82:85]
	v_mfma_f32_16x16x128_f8f6f4 v[78:81], v[220:227], v[204:211], v[78:81]
	s_setprio 0
	s_barrier
	ds_read_b128 v[180:183], v176 offset:49152
	ds_read_b128 v[184:187], v176 offset:50176
	ds_read_b128 v[188:191], v176 offset:51200
	ds_read_b128 v[192:195], v176 offset:52224
	ds_read_b128 v[196:199], v176 offset:53248
	ds_read_b128 v[200:203], v176 offset:54272
	ds_read_b128 v[204:207], v176 offset:55296
	ds_read_b128 v[208:211], v176 offset:56320
	s_mov_b32 m0, s58
	v_lshl_add_u64 v[6:7], v[6:7], 0, s[4:5]
	global_load_lds_dwordx4 v[6:7], off
	v_lshl_add_u64 v[6:7], v[8:9], 0, s[4:5]
	s_mov_b32 m0, s59
	s_nop 0
	global_load_lds_dwordx4 v[6:7], off
	s_mov_b32 m0, s44
	v_lshl_add_u64 v[2:3], v[2:3], 0, s[4:5]
	global_load_lds_dwordx4 v[2:3], off
	v_lshl_add_u64 v[2:3], v[4:5], 0, s[4:5]
	s_mov_b32 m0, s45
	s_nop 0
	global_load_lds_dwordx4 v[2:3], off
	s_add_u32 s28, s28, 0x40080
	s_addc_u32 s29, s29, 0
	s_mov_b32 m0, s60
	v_lshl_add_u64 v[2:3], s[28:29], 0, v[154:155]
	global_load_lds_dwordx4 v[2:3], off
	v_lshl_add_u64 v[2:3], s[28:29], 0, v[150:151]
	s_mov_b32 m0, s61
	s_nop 0
	global_load_lds_dwordx4 v[2:3], off
	s_waitcnt vmcnt(8) lgkmcnt(0)
	s_barrier
	s_setprio 1
	v_mfma_f32_16x16x128_f8f6f4 v[94:97], v[10:17], v[180:187], v[94:97]
	v_mfma_f32_16x16x128_f8f6f4 v[86:89], v[166:173], v[180:187], v[86:89]
	v_mfma_f32_16x16x128_f8f6f4 v[66:69], v[10:17], v[188:195], v[66:69]
	v_mfma_f32_16x16x128_f8f6f4 v[54:57], v[166:173], v[188:195], v[54:57]
	v_mfma_f32_16x16x128_f8f6f4 v[46:49], v[10:17], v[196:203], v[46:49]
	v_mfma_f32_16x16x128_f8f6f4 v[38:41], v[166:173], v[196:203], v[38:41]
	v_mfma_f32_16x16x128_f8f6f4 v[30:33], v[10:17], v[204:211], v[30:33]
	v_mfma_f32_16x16x128_f8f6f4 v[22:25], v[166:173], v[204:211], v[22:25]
	v_mfma_f32_16x16x128_f8f6f4 v[106:109], v[212:219], v[180:187], v[106:109]
	v_mfma_f32_16x16x128_f8f6f4 v[102:105], v[220:227], v[180:187], v[102:105]
	v_mfma_f32_16x16x128_f8f6f4 v[74:77], v[212:219], v[188:195], v[74:77]
	v_mfma_f32_16x16x128_f8f6f4 v[62:65], v[220:227], v[188:195], v[62:65]
	v_mfma_f32_16x16x128_f8f6f4 v[50:53], v[212:219], v[196:203], v[50:53]
	v_mfma_f32_16x16x128_f8f6f4 v[42:45], v[220:227], v[196:203], v[42:45]
	v_mfma_f32_16x16x128_f8f6f4 v[34:37], v[212:219], v[204:211], v[34:37]
	v_mfma_f32_16x16x128_f8f6f4 v[26:29], v[220:227], v[204:211], v[26:29]
	s_setprio 0
	s_add_i32 s64, s64, 2
	s_add_u32 s8, s8, 0x100
	s_addc_u32 s9, s9, 0
	s_add_u32 s62, s62, 0x100
	s_addc_u32 s63, s63, 0
	s_cmp_gt_u32 s64, 13
	s_barrier
	s_cbranch_scc0 .LBB0_215
	v_readfirstlane_b32 s99, v0
	s_cmpk_gt_u32 s99, 0xff
	s_cbranch_scc1 .Lz0_215
	s_barrier
.Lz0_215:
	v_mov_b32_e32 v166, v0
	s_nop 15
	s_nop 15
	s_lshl_b32 s9, s26, 8
	v_readfirstlane_b32 s8, v166
	s_ashr_i32 s13, s8, 2
	s_andn2_b32 s13, s13, 63
	s_lshr_b32 s8, s8, 1
	s_add_i32 s13, s13, s9
	s_and_b32 s8, s8, 0x60
	s_lshl_b32 s9, s50, 8
	v_and_or_b32 v178, v166, 15, s13
	v_lshrrev_b32_e32 v166, 1, v166
	s_or_b32 s8, s8, s9
	v_and_or_b32 v168, v166, 24, s8
	v_mov_b64_e32 v[14:15], v[18:19]
	v_mov_b64_e32 v[10:11], v[18:19]
	v_mov_b64_e32 v[6:7], v[18:19]
	v_mov_b64_e32 v[2:3], v[18:19]
	v_ashrrev_i32_e32 v169, 31, v168
	v_mov_b64_e32 v[166:167], s[2:3]
	v_mov_b64_e32 v[16:17], v[20:21]
	v_mov_b64_e32 v[12:13], v[20:21]
	v_mov_b64_e32 v[8:9], v[20:21]
	v_mov_b64_e32 v[4:5], v[20:21]
	v_mad_i64_i32 v[170:171], s[8:9], v178, s49, v[166:167]
	v_lshlrev_b64 v[168:169], 1, v[168:169]
	s_waitcnt vmcnt(6)
	v_lshl_add_u64 v[170:171], v[170:171], 0, v[168:169]
	v_pk_fma_f32 v[140:141], v[140:141], s[18:19], v[16:17] op_sel_hi:[1,0,1]
	v_pk_fma_f32 v[138:139], v[138:139], s[18:19], v[14:15] op_sel_hi:[1,0,1]
	v_pk_fma_f32 v[172:173], v[136:137], s[18:19], v[12:13] op_sel_hi:[1,0,1]
	v_pk_fma_f32 v[136:137], v[134:135], s[18:19], v[10:11] op_sel_hi:[1,0,1]
	v_cvt_pk_bf16_f32 v134, v138, v139
	v_cvt_pk_bf16_f32 v135, v140, v141
	v_pk_fma_f32 v[138:139], v[144:145], s[18:19], v[4:5] op_sel_hi:[1,0,1]
	v_cvt_pk_bf16_f32 v136, v136, v137
	v_cvt_pk_bf16_f32 v137, v172, v173
	global_store_dwordx4 v[170:171], v[134:137], off
	v_pk_fma_f32 v[140:141], v[142:143], s[18:19], v[2:3] op_sel_hi:[1,0,1]
	v_pk_fma_f32 v[124:125], v[124:125], s[18:19], v[16:17] op_sel_hi:[1,0,1]
	v_pk_fma_f32 v[134:135], v[146:147], s[18:19], v[6:7] op_sel_hi:[1,0,1]
	v_pk_fma_f32 v[136:137], v[148:149], s[18:19], v[8:9] op_sel_hi:[1,0,1]
	v_cvt_pk_bf16_f32 v134, v134, v135
	v_pk_fma_f32 v[122:123], v[122:123], s[18:19], v[14:15] op_sel_hi:[1,0,1]
	v_cvt_pk_bf16_f32 v135, v136, v137
	v_cvt_pk_bf16_f32 v136, v140, v141
	v_cvt_pk_bf16_f32 v137, v138, v139
	global_store_dwordx4 v[170:171], v[134:137], off offset:256
	v_pk_fma_f32 v[100:101], v[100:101], s[18:19], v[16:17] op_sel_hi:[1,0,1]
	v_pk_fma_f32 v[98:99], v[98:99], s[18:19], v[14:15] op_sel_hi:[1,0,1]
	v_or_b32_e32 v134, 16, v178
	v_mad_i64_i32 v[134:135], s[8:9], v134, s49, v[166:167]
	v_lshl_add_u64 v[134:135], v[134:135], 0, v[168:169]
	v_pk_fma_f32 v[136:137], v[120:121], s[18:19], v[12:13] op_sel_hi:[1,0,1]
	v_pk_fma_f32 v[120:121], v[118:119], s[18:19], v[10:11] op_sel_hi:[1,0,1]
	v_cvt_pk_bf16_f32 v118, v122, v123
	v_cvt_pk_bf16_f32 v119, v124, v125
	v_pk_fma_f32 v[122:123], v[128:129], s[18:19], v[4:5] op_sel_hi:[1,0,1]
	v_cvt_pk_bf16_f32 v120, v120, v121
	v_cvt_pk_bf16_f32 v121, v136, v137
	global_store_dwordx4 v[134:135], v[118:121], off
	v_pk_fma_f32 v[124:125], v[126:127], s[18:19], v[2:3] op_sel_hi:[1,0,1]
	v_pk_fma_f32 v[72:73], v[72:73], s[18:19], v[16:17] op_sel_hi:[1,0,1]
	v_pk_fma_f32 v[118:119], v[130:131], s[18:19], v[6:7] op_sel_hi:[1,0,1]
	v_pk_fma_f32 v[120:121], v[132:133], s[18:19], v[8:9] op_sel_hi:[1,0,1]
	v_cvt_pk_bf16_f32 v118, v118, v119
	v_pk_fma_f32 v[70:71], v[70:71], s[18:19], v[14:15] op_sel_hi:[1,0,1]
	v_cvt_pk_bf16_f32 v119, v120, v121
	v_cvt_pk_bf16_f32 v120, v124, v125
	v_cvt_pk_bf16_f32 v121, v122, v123
	global_store_dwordx4 v[134:135], v[118:121], off offset:256
	v_pk_fma_f32 v[66:67], v[66:67], s[18:19], v[14:15] op_sel_hi:[1,0,1]
	v_pk_fma_f32 v[62:63], v[62:63], s[18:19], v[2:3] op_sel_hi:[1,0,1]
	v_or_b32_e32 v118, 32, v178
	v_mad_i64_i32 v[118:119], s[8:9], v118, s49, v[166:167]
	v_lshl_add_u64 v[118:119], v[118:119], 0, v[168:169]
	v_pk_fma_f32 v[120:121], v[92:93], s[18:19], v[12:13] op_sel_hi:[1,0,1]
	v_pk_fma_f32 v[92:93], v[90:91], s[18:19], v[10:11] op_sel_hi:[1,0,1]
	v_cvt_pk_bf16_f32 v90, v98, v99
	v_cvt_pk_bf16_f32 v91, v100, v101
	v_pk_fma_f32 v[98:99], v[112:113], s[18:19], v[4:5] op_sel_hi:[1,0,1]
	v_cvt_pk_bf16_f32 v92, v92, v93
	v_cvt_pk_bf16_f32 v93, v120, v121
	global_store_dwordx4 v[118:119], v[90:93], off
	v_pk_fma_f32 v[100:101], v[110:111], s[18:19], v[2:3] op_sel_hi:[1,0,1]
	v_pk_fma_f32 v[48:49], v[48:49], s[18:19], v[16:17] op_sel_hi:[1,0,1]
	v_pk_fma_f32 v[90:91], v[114:115], s[18:19], v[6:7] op_sel_hi:[1,0,1]
	v_pk_fma_f32 v[92:93], v[116:117], s[18:19], v[8:9] op_sel_hi:[1,0,1]
	v_cvt_pk_bf16_f32 v90, v90, v91
	v_pk_fma_f32 v[46:47], v[46:47], s[18:19], v[14:15] op_sel_hi:[1,0,1]
	v_cvt_pk_bf16_f32 v91, v92, v93
	v_cvt_pk_bf16_f32 v92, v100, v101
	v_cvt_pk_bf16_f32 v93, v98, v99
	global_store_dwordx4 v[118:119], v[90:93], off offset:256
	v_pk_fma_f32 v[44:45], v[44:45], s[18:19], v[4:5] op_sel_hi:[1,0,1]
	v_pk_fma_f32 v[42:43], v[42:43], s[18:19], v[2:3] op_sel_hi:[1,0,1]
	v_or_b32_e32 v90, 48, v178
	v_mad_i64_i32 v[90:91], s[8:9], v90, s49, v[166:167]
	v_lshl_add_u64 v[90:91], v[90:91], 0, v[168:169]
	v_pk_fma_f32 v[92:93], v[60:61], s[18:19], v[12:13] op_sel_hi:[1,0,1]
	v_pk_fma_f32 v[60:61], v[58:59], s[18:19], v[10:11] op_sel_hi:[1,0,1]
	v_cvt_pk_bf16_f32 v58, v70, v71
	v_cvt_pk_bf16_f32 v59, v72, v73
	v_pk_fma_f32 v[70:71], v[80:81], s[18:19], v[4:5] op_sel_hi:[1,0,1]
	v_cvt_pk_bf16_f32 v60, v60, v61
	v_cvt_pk_bf16_f32 v61, v92, v93
	global_store_dwordx4 v[90:91], v[58:61], off
	v_pk_fma_f32 v[72:73], v[78:79], s[18:19], v[2:3] op_sel_hi:[1,0,1]
	v_pk_fma_f32 v[78:79], v[86:87], s[18:19], v[10:11] op_sel_hi:[1,0,1]
	v_pk_fma_f32 v[58:59], v[82:83], s[18:19], v[6:7] op_sel_hi:[1,0,1]
	v_pk_fma_f32 v[60:61], v[84:85], s[18:19], v[8:9] op_sel_hi:[1,0,1]
	v_cvt_pk_bf16_f32 v58, v58, v59
	v_pk_fma_f32 v[24:25], v[24:25], s[18:19], v[12:13] op_sel_hi:[1,0,1]
	v_cvt_pk_bf16_f32 v59, v60, v61
	v_cvt_pk_bf16_f32 v60, v72, v73
	v_cvt_pk_bf16_f32 v61, v70, v71
	global_store_dwordx4 v[90:91], v[58:61], off offset:256
	v_pk_fma_f32 v[72:73], v[88:89], s[18:19], v[12:13] op_sel_hi:[1,0,1]
	s_and_b64 vcc, exec, s[6:7]
	v_add_u32_e32 v58, 0x80, v178
	v_mad_i64_i32 v[58:59], s[8:9], v58, s49, v[166:167]
	v_lshl_add_u64 v[70:71], v[58:59], 0, v[168:169]
	v_pk_fma_f32 v[58:59], v[94:95], s[18:19], v[14:15] op_sel_hi:[1,0,1]
	v_pk_fma_f32 v[60:61], v[96:97], s[18:19], v[16:17] op_sel_hi:[1,0,1]
	v_cvt_pk_bf16_f32 v58, v58, v59
	v_pk_fma_f32 v[14:15], v[30:31], s[18:19], v[14:15] op_sel_hi:[1,0,1]
	v_cvt_pk_bf16_f32 v59, v60, v61
	v_cvt_pk_bf16_f32 v60, v78, v79
	v_cvt_pk_bf16_f32 v61, v72, v73
	global_store_dwordx4 v[70:71], v[58:61], off
	v_pk_fma_f32 v[72:73], v[104:105], s[18:19], v[4:5] op_sel_hi:[1,0,1]
	v_pk_fma_f32 v[78:79], v[102:103], s[18:19], v[2:3] op_sel_hi:[1,0,1]
	v_pk_fma_f32 v[58:59], v[106:107], s[18:19], v[6:7] op_sel_hi:[1,0,1]
	v_pk_fma_f32 v[60:61], v[108:109], s[18:19], v[8:9] op_sel_hi:[1,0,1]
	v_cvt_pk_bf16_f32 v58, v58, v59
	s_mov_b32 s50, s14
	v_cvt_pk_bf16_f32 v59, v60, v61
	v_cvt_pk_bf16_f32 v60, v78, v79
	v_cvt_pk_bf16_f32 v61, v72, v73
	global_store_dwordx4 v[70:71], v[58:61], off offset:256
	s_mov_b32 s26, s20
	s_mov_b64 s[28:29], s[24:25]
	v_add_u32_e32 v58, 0x90, v178
	v_mad_i64_i32 v[58:59], s[8:9], v58, s49, v[166:167]
	v_lshl_add_u64 v[58:59], v[58:59], 0, v[168:169]
	v_pk_fma_f32 v[60:61], v[68:69], s[18:19], v[16:17] op_sel_hi:[1,0,1]
	v_pk_fma_f32 v[68:69], v[56:57], s[18:19], v[12:13] op_sel_hi:[1,0,1]
	v_pk_fma_f32 v[56:57], v[54:55], s[18:19], v[10:11] op_sel_hi:[1,0,1]
	v_cvt_pk_bf16_f32 v54, v66, v67
	v_cvt_pk_bf16_f32 v55, v60, v61
	v_pk_fma_f32 v[60:61], v[64:65], s[18:19], v[4:5] op_sel_hi:[1,0,1]
	v_cvt_pk_bf16_f32 v56, v56, v57
	v_cvt_pk_bf16_f32 v57, v68, v69
	global_store_dwordx4 v[58:59], v[54:57], off
	v_pk_fma_f32 v[16:17], v[32:33], s[18:19], v[16:17] op_sel_hi:[1,0,1]
	s_mov_b64 s[30:31], s[22:23]
	v_pk_fma_f32 v[54:55], v[74:75], s[18:19], v[6:7] op_sel_hi:[1,0,1]
	v_pk_fma_f32 v[56:57], v[76:77], s[18:19], v[8:9] op_sel_hi:[1,0,1]
	v_cvt_pk_bf16_f32 v54, v54, v55
	v_readlane_b32 s72, v254, 51
	v_cvt_pk_bf16_f32 v55, v56, v57
	v_cvt_pk_bf16_f32 v56, v62, v63
	v_cvt_pk_bf16_f32 v57, v60, v61
	global_store_dwordx4 v[58:59], v[54:57], off offset:256
	v_readlane_b32 s73, v254, 52
	s_nop 0
	v_add_u32_e32 v54, 0xa0, v178
	v_mad_i64_i32 v[54:55], s[8:9], v54, s49, v[166:167]
	v_lshl_add_u64 v[54:55], v[54:55], 0, v[168:169]
	v_pk_fma_f32 v[56:57], v[40:41], s[18:19], v[12:13] op_sel_hi:[1,0,1]
	v_pk_fma_f32 v[40:41], v[38:39], s[18:19], v[10:11] op_sel_hi:[1,0,1]
	v_cvt_pk_bf16_f32 v38, v46, v47
	v_cvt_pk_bf16_f32 v39, v48, v49
	v_pk_fma_f32 v[12:13], v[22:23], s[18:19], v[10:11] op_sel_hi:[1,0,1]
	v_cvt_pk_bf16_f32 v40, v40, v41
	v_cvt_pk_bf16_f32 v41, v56, v57
	global_store_dwordx4 v[54:55], v[38:41], off
	s_nop 1
	v_pk_fma_f32 v[38:39], v[50:51], s[18:19], v[6:7] op_sel_hi:[1,0,1]
	v_pk_fma_f32 v[40:41], v[52:53], s[18:19], v[8:9] op_sel_hi:[1,0,1]
	v_cvt_pk_bf16_f32 v38, v38, v39
	v_pk_fma_f32 v[8:9], v[36:37], s[18:19], v[8:9] op_sel_hi:[1,0,1]
	v_cvt_pk_bf16_f32 v39, v40, v41
	v_cvt_pk_bf16_f32 v40, v42, v43
	v_cvt_pk_bf16_f32 v41, v44, v45
	global_store_dwordx4 v[54:55], v[38:41], off offset:256
	v_cvt_pk_bf16_f32 v10, v14, v15
	v_cvt_pk_bf16_f32 v11, v16, v17
	v_cvt_pk_bf16_f32 v12, v12, v13
	v_cvt_pk_bf16_f32 v13, v24, v25
	v_pk_fma_f32 v[6:7], v[34:35], s[18:19], v[6:7] op_sel_hi:[1,0,1]
	s_nop 0
	v_add_u32_e32 v38, 0xb0, v178
	v_mad_i64_i32 v[38:39], s[8:9], v38, s49, v[166:167]
	v_lshl_add_u64 v[38:39], v[38:39], 0, v[168:169]
	global_store_dwordx4 v[38:39], v[10:13], off
	s_nop 1
	v_pk_fma_f32 v[10:11], v[28:29], s[18:19], v[4:5] op_sel_hi:[1,0,1]
	v_pk_fma_f32 v[4:5], v[26:27], s[18:19], v[2:3] op_sel_hi:[1,0,1]
	v_cvt_pk_bf16_f32 v2, v6, v7
	v_cvt_pk_bf16_f32 v3, v8, v9
	s_nop 0
	v_cvt_pk_bf16_f32 v4, v4, v5
	v_cvt_pk_bf16_f32 v5, v10, v11
	global_store_dwordx4 v[38:39], v[2:5], off offset:256
	v_readfirstlane_b32 s99, v0
	s_cmpk_gt_u32 s99, 0xff
	s_cbranch_scc0 .Lz1_215
	s_barrier
.Lz1_215:
	s_cbranch_vccz .LBB0_212
	s_waitcnt vmcnt(0)
	v_readlane_b32 s44, v254, 43
	v_readlane_b32 s45, v254, 44
	s_cmpk_gt_u32 s19, 0xff
	s_mov_b64 s[52:53], s[44:45]
	v_readlane_b32 s46, v254, 45
	v_readlane_b32 s47, v254, 46
	s_cbranch_scc1 .LBB0_219
	s_barrier

.LBB0_1106:
	ds_read_b128 v[168:171], v164
	ds_read_b128 v[172:175], v164 offset:1024
	ds_read_b128 v[176:179], v164 offset:2048
	ds_read_b128 v[180:183], v164 offset:3072
	s_add_u32 s30, s28, 0xfff80080
	s_addc_u32 s31, s29, -1
	s_cmp_eq_u32 s64, 28
	s_cselect_b32 s35, s7, s31
	s_cselect_b32 s34, s60, s30
	s_cselect_b32 s31, s21, s63
	s_cselect_b32 s30, s61, s62
	v_lshl_add_u64 v[162:163], s[28:29], 0, v[154:155]
	s_add_i32 m0, s45, 0xc000
	ds_read_b128 v[184:187], v165
	ds_read_b128 v[188:191], v165 offset:1024
	ds_read_b128 v[192:195], v165 offset:2048
	ds_read_b128 v[196:199], v165 offset:3072
	ds_read_b128 v[200:203], v165 offset:4096
	ds_read_b128 v[204:207], v165 offset:5120
	ds_read_b128 v[208:211], v165 offset:6144
	ds_read_b128 v[212:215], v165 offset:7168
	global_load_lds_dwordx4 v[162:163], off
	v_lshl_add_u64 v[162:163], s[28:29], 0, v[156:157]
	s_add_i32 m0, s45, 0xe000
	s_nop 0
	global_load_lds_dwordx4 v[162:163], off
	s_waitcnt lgkmcnt(8)
	s_barrier
	s_waitcnt lgkmcnt(0)
	s_setprio 1
	s_waitcnt lgkmcnt(0)
	v_mfma_f32_16x16x32_bf16 v[142:145], v[168:171], v[184:187], v[142:145]
	v_mfma_f32_16x16x32_bf16 v[138:141], v[176:179], v[184:187], v[138:141]
	v_mfma_f32_16x16x32_bf16 v[126:129], v[168:171], v[192:195], v[126:129]
	v_mfma_f32_16x16x32_bf16 v[122:125], v[176:179], v[192:195], v[122:125]
	v_mfma_f32_16x16x32_bf16 v[110:113], v[168:171], v[200:203], v[110:113]
	v_mfma_f32_16x16x32_bf16 v[106:109], v[176:179], v[200:203], v[106:109]
	v_mfma_f32_16x16x32_bf16 v[94:97], v[168:171], v[208:211], v[94:97]
	v_mfma_f32_16x16x32_bf16 v[90:93], v[176:179], v[208:211], v[90:93]
	v_mfma_f32_16x16x32_bf16 v[142:145], v[172:175], v[188:191], v[142:145]
	v_mfma_f32_16x16x32_bf16 v[138:141], v[180:183], v[188:191], v[138:141]
	v_mfma_f32_16x16x32_bf16 v[126:129], v[172:175], v[196:199], v[126:129]
	v_mfma_f32_16x16x32_bf16 v[122:125], v[180:183], v[196:199], v[122:125]
	v_mfma_f32_16x16x32_bf16 v[110:113], v[172:175], v[204:207], v[110:113]
	v_mfma_f32_16x16x32_bf16 v[106:109], v[180:183], v[204:207], v[106:109]
	v_mfma_f32_16x16x32_bf16 v[94:97], v[172:175], v[212:215], v[94:97]
	v_mfma_f32_16x16x32_bf16 v[90:93], v[180:183], v[212:215], v[90:93]
	s_setprio 0
	s_barrier
	s_add_i32 s65, s53, s44
	v_lshl_add_u64 v[162:163], s[30:31], 0, v[148:149]
	s_mov_b32 m0, s65
	ds_read_b128 v[216:219], v166
	ds_read_b128 v[220:223], v166 offset:1024
	ds_read_b128 v[224:227], v166 offset:2048
	ds_read_b128 v[228:231], v166 offset:3072
	global_load_lds_dwordx4 v[162:163], off
	v_lshl_add_u64 v[232:233], s[30:31], 0, v[152:153]
	s_add_i32 m0, s65, 0x2000
	s_nop 0
	global_load_lds_dwordx4 v[232:233], off
	s_barrier
	s_waitcnt lgkmcnt(0)
	s_setprio 1
	s_waitcnt lgkmcnt(0)
	v_mfma_f32_16x16x32_bf16 v[134:137], v[216:219], v[184:187], v[134:137]
	v_mfma_f32_16x16x32_bf16 v[130:133], v[224:227], v[184:187], v[130:133]
	v_mfma_f32_16x16x32_bf16 v[118:121], v[216:219], v[192:195], v[118:121]
	v_mfma_f32_16x16x32_bf16 v[114:117], v[224:227], v[192:195], v[114:117]
	v_mfma_f32_16x16x32_bf16 v[102:105], v[216:219], v[200:203], v[102:105]
	v_mfma_f32_16x16x32_bf16 v[98:101], v[224:227], v[200:203], v[98:101]
	v_mfma_f32_16x16x32_bf16 v[86:89], v[216:219], v[208:211], v[86:89]
	v_mfma_f32_16x16x32_bf16 v[82:85], v[224:227], v[208:211], v[82:85]
	v_mfma_f32_16x16x32_bf16 v[134:137], v[220:223], v[188:191], v[134:137]
	v_mfma_f32_16x16x32_bf16 v[130:133], v[228:231], v[188:191], v[130:133]
	v_mfma_f32_16x16x32_bf16 v[118:121], v[220:223], v[196:199], v[118:121]
	v_mfma_f32_16x16x32_bf16 v[114:117], v[228:231], v[196:199], v[114:117]
	v_mfma_f32_16x16x32_bf16 v[102:105], v[220:223], v[204:207], v[102:105]
	v_mfma_f32_16x16x32_bf16 v[98:101], v[228:231], v[204:207], v[98:101]
	v_mfma_f32_16x16x32_bf16 v[86:89], v[220:223], v[212:215], v[86:89]
	v_mfma_f32_16x16x32_bf16 v[82:85], v[228:231], v[212:215], v[82:85]
	s_setprio 0
	s_mov_b32 m0, s45
	v_lshl_add_u64 v[234:235], s[34:35], 0, v[146:147]
	s_barrier
	ds_read_b128 v[184:187], v165 offset:16384
	ds_read_b128 v[188:191], v165 offset:17408
	ds_read_b128 v[192:195], v165 offset:18432
	ds_read_b128 v[196:199], v165 offset:19456
	ds_read_b128 v[200:203], v165 offset:20480
	ds_read_b128 v[204:207], v165 offset:21504
	ds_read_b128 v[208:211], v165 offset:22528
	ds_read_b128 v[212:215], v165 offset:23552
	global_load_lds_dwordx4 v[234:235], off
	v_lshl_add_u64 v[236:237], s[34:35], 0, v[150:151]
	s_mov_b32 m0, s46
	s_nop 0
	global_load_lds_dwordx4 v[236:237], off
	s_barrier
	s_waitcnt lgkmcnt(0)
	s_setprio 1
	s_waitcnt lgkmcnt(0)
	v_mfma_f32_16x16x32_bf16 v[78:81], v[168:171], v[184:187], v[78:81]
	v_mfma_f32_16x16x32_bf16 v[74:77], v[176:179], v[184:187], v[74:77]
	v_mfma_f32_16x16x32_bf16 v[66:69], v[168:171], v[192:195], v[66:69]
	v_mfma_f32_16x16x32_bf16 v[58:61], v[176:179], v[192:195], v[58:61]
	v_mfma_f32_16x16x32_bf16 v[50:53], v[168:171], v[200:203], v[50:53]
	v_mfma_f32_16x16x32_bf16 v[42:45], v[176:179], v[200:203], v[42:45]
	v_mfma_f32_16x16x32_bf16 v[34:37], v[168:171], v[208:211], v[34:37]
	v_mfma_f32_16x16x32_bf16 v[26:29], v[176:179], v[208:211], v[26:29]
	v_mfma_f32_16x16x32_bf16 v[78:81], v[172:175], v[188:191], v[78:81]
	v_mfma_f32_16x16x32_bf16 v[74:77], v[180:183], v[188:191], v[74:77]
	v_mfma_f32_16x16x32_bf16 v[66:69], v[172:175], v[196:199], v[66:69]
	v_mfma_f32_16x16x32_bf16 v[58:61], v[180:183], v[196:199], v[58:61]
	v_mfma_f32_16x16x32_bf16 v[50:53], v[172:175], v[204:207], v[50:53]
	v_mfma_f32_16x16x32_bf16 v[42:45], v[180:183], v[204:207], v[42:45]
	v_mfma_f32_16x16x32_bf16 v[34:37], v[172:175], v[212:215], v[34:37]
	v_mfma_f32_16x16x32_bf16 v[26:29], v[180:183], v[212:215], v[26:29]
	s_setprio 0
	s_barrier
	s_add_u32 s66, s30, 0x80000
	s_addc_u32 s67, s31, 0
	s_add_i32 s65, s54, s44
	v_lshl_add_u64 v[168:169], s[66:67], 0, v[148:149]
	s_mov_b32 m0, s65
	s_nop 0
	global_load_lds_dwordx4 v[168:169], off
	v_lshl_add_u64 v[168:169], s[66:67], 0, v[152:153]
	s_add_i32 m0, s65, 0x2000
	s_nop 0
	global_load_lds_dwordx4 v[168:169], off
	s_waitcnt vmcnt(6)
	s_barrier
	s_setprio 1
	v_mfma_f32_16x16x32_bf16 v[70:73], v[216:219], v[184:187], v[70:73]
	v_mfma_f32_16x16x32_bf16 v[62:65], v[224:227], v[184:187], v[62:65]
	v_mfma_f32_16x16x32_bf16 v[54:57], v[216:219], v[192:195], v[54:57]
	v_mfma_f32_16x16x32_bf16 v[46:49], v[224:227], v[192:195], v[46:49]
	v_mfma_f32_16x16x32_bf16 v[38:41], v[216:219], v[200:203], v[38:41]
	v_mfma_f32_16x16x32_bf16 v[30:33], v[224:227], v[200:203], v[30:33]
	v_mfma_f32_16x16x32_bf16 v[22:25], v[216:219], v[208:211], v[22:25]
	v_mfma_f32_16x16x32_bf16 v[18:21], v[224:227], v[208:211], v[18:21]
	v_mfma_f32_16x16x32_bf16 v[70:73], v[220:223], v[188:191], v[70:73]
	v_mfma_f32_16x16x32_bf16 v[62:65], v[228:231], v[188:191], v[62:65]
	v_mfma_f32_16x16x32_bf16 v[54:57], v[220:223], v[196:199], v[54:57]
	v_mfma_f32_16x16x32_bf16 v[46:49], v[228:231], v[196:199], v[46:49]
	v_mfma_f32_16x16x32_bf16 v[38:41], v[220:223], v[204:207], v[38:41]
	v_mfma_f32_16x16x32_bf16 v[30:33], v[228:231], v[204:207], v[30:33]
	v_mfma_f32_16x16x32_bf16 v[22:25], v[220:223], v[212:215], v[22:25]
	v_mfma_f32_16x16x32_bf16 v[18:21], v[228:231], v[212:215], v[18:21]
	s_setprio 0
	s_add_i32 s65, 0, 0x18000
	v_add_u32_e32 v167, s65, v1
	s_barrier
	ds_read_b128 v[168:171], v167
	ds_read_b128 v[172:175], v167 offset:1024
	ds_read_b128 v[176:179], v167 offset:2048
	ds_read_b128 v[180:183], v167 offset:3072
	s_add_u32 s34, s34, 0x80000
	s_addc_u32 s35, s35, 0
	s_mov_b32 m0, s47
	v_lshl_add_u64 v[216:217], s[34:35], 0, v[146:147]
	ds_read_b128 v[184:187], v165 offset:32768
	ds_read_b128 v[188:191], v165 offset:33792
	ds_read_b128 v[192:195], v165 offset:34816
	ds_read_b128 v[196:199], v165 offset:35840
	ds_read_b128 v[200:203], v165 offset:36864
	ds_read_b128 v[204:207], v165 offset:37888
	ds_read_b128 v[208:211], v165 offset:38912
	ds_read_b128 v[212:215], v165 offset:39936
	global_load_lds_dwordx4 v[216:217], off
	v_lshl_add_u64 v[216:217], s[34:35], 0, v[150:151]
	s_mov_b32 m0, s48
	s_nop 0
	global_load_lds_dwordx4 v[216:217], off
	s_waitcnt lgkmcnt(8)
	s_barrier
	s_waitcnt lgkmcnt(0)
	s_setprio 1
	s_waitcnt lgkmcnt(0)
	v_mfma_f32_16x16x32_bf16 v[142:145], v[168:171], v[184:187], v[142:145]
	v_mfma_f32_16x16x32_bf16 v[138:141], v[176:179], v[184:187], v[138:141]
	v_mfma_f32_16x16x32_bf16 v[126:129], v[168:171], v[192:195], v[126:129]
	v_mfma_f32_16x16x32_bf16 v[122:125], v[176:179], v[192:195], v[122:125]
	v_mfma_f32_16x16x32_bf16 v[110:113], v[168:171], v[200:203], v[110:113]
	v_mfma_f32_16x16x32_bf16 v[106:109], v[176:179], v[200:203], v[106:109]
	v_mfma_f32_16x16x32_bf16 v[94:97], v[168:171], v[208:211], v[94:97]
	v_mfma_f32_16x16x32_bf16 v[90:93], v[176:179], v[208:211], v[90:93]
	v_mfma_f32_16x16x32_bf16 v[142:145], v[172:175], v[188:191], v[142:145]
	v_mfma_f32_16x16x32_bf16 v[138:141], v[180:183], v[188:191], v[138:141]
	v_mfma_f32_16x16x32_bf16 v[126:129], v[172:175], v[196:199], v[126:129]
	v_mfma_f32_16x16x32_bf16 v[122:125], v[180:183], v[196:199], v[122:125]
	v_mfma_f32_16x16x32_bf16 v[110:113], v[172:175], v[204:207], v[110:113]
	v_mfma_f32_16x16x32_bf16 v[106:109], v[180:183], v[204:207], v[106:109]
	v_mfma_f32_16x16x32_bf16 v[94:97], v[172:175], v[212:215], v[94:97]
	v_mfma_f32_16x16x32_bf16 v[90:93], v[180:183], v[212:215], v[90:93]
	s_setprio 0
	s_barrier
	s_add_i32 s34, 0, 0x1c000
	s_add_i32 s35, s65, s44
	v_add_u32_e32 v167, s34, v1
	v_lshl_add_u64 v[162:163], v[162:163], 0, s[10:11]
	s_mov_b32 m0, s35
	ds_read_b128 v[216:219], v167
	ds_read_b128 v[220:223], v167 offset:1024
	ds_read_b128 v[224:227], v167 offset:2048
	ds_read_b128 v[228:231], v167 offset:3072
	global_load_lds_dwordx4 v[162:163], off
	v_lshl_add_u64 v[162:163], v[232:233], 0, s[10:11]
	s_add_i32 m0, s35, 0x2000
	s_nop 0
	global_load_lds_dwordx4 v[162:163], off
	s_barrier
	s_waitcnt lgkmcnt(0)
	s_setprio 1
	s_waitcnt lgkmcnt(0)
	v_mfma_f32_16x16x32_bf16 v[134:137], v[216:219], v[184:187], v[134:137]
	v_mfma_f32_16x16x32_bf16 v[130:133], v[224:227], v[184:187], v[130:133]
	v_mfma_f32_16x16x32_bf16 v[118:121], v[216:219], v[192:195], v[118:121]
	v_mfma_f32_16x16x32_bf16 v[114:117], v[224:227], v[192:195], v[114:117]
	v_mfma_f32_16x16x32_bf16 v[102:105], v[216:219], v[200:203], v[102:105]
	v_mfma_f32_16x16x32_bf16 v[98:101], v[224:227], v[200:203], v[98:101]
	v_mfma_f32_16x16x32_bf16 v[86:89], v[216:219], v[208:211], v[86:89]
	v_mfma_f32_16x16x32_bf16 v[82:85], v[224:227], v[208:211], v[82:85]
	v_mfma_f32_16x16x32_bf16 v[134:137], v[220:223], v[188:191], v[134:137]
	v_mfma_f32_16x16x32_bf16 v[130:133], v[228:231], v[188:191], v[130:133]
	v_mfma_f32_16x16x32_bf16 v[118:121], v[220:223], v[196:199], v[118:121]
	v_mfma_f32_16x16x32_bf16 v[114:117], v[228:231], v[196:199], v[114:117]
	v_mfma_f32_16x16x32_bf16 v[102:105], v[220:223], v[204:207], v[102:105]
	v_mfma_f32_16x16x32_bf16 v[98:101], v[228:231], v[204:207], v[98:101]
	v_mfma_f32_16x16x32_bf16 v[86:89], v[220:223], v[212:215], v[86:89]
	v_mfma_f32_16x16x32_bf16 v[82:85], v[228:231], v[212:215], v[82:85]
	s_setprio 0
	s_mov_b32 m0, s50
	v_lshl_add_u64 v[162:163], v[234:235], 0, s[10:11]
	s_barrier
	ds_read_b128 v[184:187], v165 offset:49152
	ds_read_b128 v[188:191], v165 offset:50176
	ds_read_b128 v[192:195], v165 offset:51200
	ds_read_b128 v[196:199], v165 offset:52224
	ds_read_b128 v[200:203], v165 offset:53248
	ds_read_b128 v[204:207], v165 offset:54272
	ds_read_b128 v[208:211], v165 offset:55296
	ds_read_b128 v[212:215], v165 offset:56320
	global_load_lds_dwordx4 v[162:163], off
	v_lshl_add_u64 v[162:163], v[236:237], 0, s[10:11]
	s_mov_b32 m0, s51
	s_nop 0
	global_load_lds_dwordx4 v[162:163], off
	s_barrier
	s_waitcnt lgkmcnt(0)
	s_setprio 1
	s_waitcnt lgkmcnt(0)
	v_mfma_f32_16x16x32_bf16 v[78:81], v[168:171], v[184:187], v[78:81]
	v_mfma_f32_16x16x32_bf16 v[74:77], v[176:179], v[184:187], v[74:77]
	v_mfma_f32_16x16x32_bf16 v[66:69], v[168:171], v[192:195], v[66:69]
	v_mfma_f32_16x16x32_bf16 v[58:61], v[176:179], v[192:195], v[58:61]
	v_mfma_f32_16x16x32_bf16 v[50:53], v[168:171], v[200:203], v[50:53]
	v_mfma_f32_16x16x32_bf16 v[42:45], v[176:179], v[200:203], v[42:45]
	v_mfma_f32_16x16x32_bf16 v[34:37], v[168:171], v[208:211], v[34:37]
	v_mfma_f32_16x16x32_bf16 v[26:29], v[176:179], v[208:211], v[26:29]
	v_mfma_f32_16x16x32_bf16 v[78:81], v[172:175], v[188:191], v[78:81]
	v_mfma_f32_16x16x32_bf16 v[74:77], v[180:183], v[188:191], v[74:77]
	v_mfma_f32_16x16x32_bf16 v[66:69], v[172:175], v[196:199], v[66:69]
	v_mfma_f32_16x16x32_bf16 v[58:61], v[180:183], v[196:199], v[58:61]
	v_mfma_f32_16x16x32_bf16 v[50:53], v[172:175], v[204:207], v[50:53]
	v_mfma_f32_16x16x32_bf16 v[42:45], v[180:183], v[204:207], v[42:45]
	v_mfma_f32_16x16x32_bf16 v[34:37], v[172:175], v[212:215], v[34:37]
	v_mfma_f32_16x16x32_bf16 v[26:29], v[180:183], v[212:215], v[26:29]
	s_setprio 0
	s_barrier
	s_add_u32 s30, s30, 0x80080
	s_addc_u32 s31, s31, 0
	s_add_i32 s34, s34, s44
	v_lshl_add_u64 v[162:163], s[30:31], 0, v[148:149]
	s_mov_b32 m0, s34
	s_nop 0
	global_load_lds_dwordx4 v[162:163], off
	v_lshl_add_u64 v[162:163], s[30:31], 0, v[152:153]
	s_add_i32 m0, s34, 0x2000
	s_nop 0
	global_load_lds_dwordx4 v[162:163], off
	s_waitcnt vmcnt(6)
	s_barrier
	s_setprio 1
	v_mfma_f32_16x16x32_bf16 v[70:73], v[216:219], v[184:187], v[70:73]
	v_mfma_f32_16x16x32_bf16 v[62:65], v[224:227], v[184:187], v[62:65]
	v_mfma_f32_16x16x32_bf16 v[54:57], v[216:219], v[192:195], v[54:57]
	v_mfma_f32_16x16x32_bf16 v[46:49], v[224:227], v[192:195], v[46:49]
	v_mfma_f32_16x16x32_bf16 v[38:41], v[216:219], v[200:203], v[38:41]
	v_mfma_f32_16x16x32_bf16 v[30:33], v[224:227], v[200:203], v[30:33]
	v_mfma_f32_16x16x32_bf16 v[22:25], v[216:219], v[208:211], v[22:25]
	v_mfma_f32_16x16x32_bf16 v[18:21], v[224:227], v[208:211], v[18:21]
	v_mfma_f32_16x16x32_bf16 v[70:73], v[220:223], v[188:191], v[70:73]
	v_mfma_f32_16x16x32_bf16 v[62:65], v[228:231], v[188:191], v[62:65]
	v_mfma_f32_16x16x32_bf16 v[54:57], v[220:223], v[196:199], v[54:57]
	v_mfma_f32_16x16x32_bf16 v[46:49], v[228:231], v[196:199], v[46:49]
	v_mfma_f32_16x16x32_bf16 v[38:41], v[220:223], v[204:207], v[38:41]
	v_mfma_f32_16x16x32_bf16 v[30:33], v[228:231], v[204:207], v[30:33]
	v_mfma_f32_16x16x32_bf16 v[22:25], v[220:223], v[212:215], v[22:25]
	v_mfma_f32_16x16x32_bf16 v[18:21], v[228:231], v[212:215], v[18:21]
	s_setprio 0
	s_add_i32 s64, s64, 2
	s_add_u32 s28, s28, 0x100
	s_addc_u32 s29, s29, 0
	s_add_u32 s62, s62, 0x100
	s_addc_u32 s63, s63, 0
	s_cmp_gt_u32 s64, 29
	s_barrier
	s_cbranch_scc0 .LBB0_1106
	v_readfirstlane_b32 s99, v0
	s_cmpk_gt_u32 s99, 0xff
	s_cbranch_scc1 .Lz0_1106
	s_barrier
.Lz0_1106:
	v_mov_b32_e32 v162, v0
	s_lshl_b32 s6, s6, 8
	v_readfirstlane_b32 s7, v162
	s_ashr_i32 s21, s7, 2
	s_andn2_b32 s21, s21, 63
	s_add_i32 s21, s21, s6
	s_lshr_b32 s7, s7, 1
	v_and_or_b32 v168, v162, 15, s21
	s_lshl_b32 s6, s59, 8
	s_and_b32 s21, s7, 0x60
	v_lshrrev_b32_e32 v162, 1, v162
	s_or_b32 s6, s21, s6
	v_and_b32_e32 v167, 24, v162
	v_or_b32_e32 v162, s6, v167
	v_ashrrev_i32_e32 v169, 31, v168
	v_ashrrev_i32_e32 v163, 31, v162
	v_lshlrev_b64 v[170:171], 13, v[168:169]
	v_lshl_add_u64 v[170:171], s[8:9], 0, v[170:171]
	v_lshlrev_b64 v[172:173], 1, v[162:163]
	s_waitcnt vmcnt(6)
	v_lshl_add_u64 v[162:163], v[170:171], 0, v[172:173]
	v_pk_mul_f32 v[144:145], v[144:145], v[12:13]
	v_pk_mul_f32 v[142:143], v[142:143], v[10:11]
	v_pk_mul_f32 v[170:171], v[140:141], v[16:17]
	v_pk_mul_f32 v[140:141], v[138:139], v[14:15]
	v_cvt_pk_bf16_f32 v138, v142, v143
	v_cvt_pk_bf16_f32 v139, v144, v145
	v_pk_mul_f32 v[134:135], v[134:135], v[2:3]
	v_cvt_pk_bf16_f32 v140, v140, v141
	v_cvt_pk_bf16_f32 v141, v170, v171
	global_store_dwordx4 v[162:163], v[138:141], off
	v_pk_mul_f32 v[136:137], v[136:137], v[4:5]
	v_pk_mul_f32 v[128:129], v[128:129], v[12:13]
	v_pk_mul_f32 v[138:139], v[132:133], v[8:9]
	v_pk_mul_f32 v[132:133], v[130:131], v[6:7]
	v_cvt_pk_bf16_f32 v130, v134, v135
	v_cvt_pk_bf16_f32 v131, v136, v137
	v_pk_mul_f32 v[126:127], v[126:127], v[10:11]
	v_cvt_pk_bf16_f32 v132, v132, v133
	v_cvt_pk_bf16_f32 v133, v138, v139
	global_store_dwordx4 v[162:163], v[130:133], off offset:256
	v_pk_mul_f32 v[118:119], v[118:119], v[2:3]
	v_pk_mul_f32 v[120:121], v[120:121], v[4:5]
	v_or_b32_e32 v130, 16, v168
	v_ashrrev_i32_e32 v131, 31, v130
	v_lshlrev_b64 v[130:131], 13, v[130:131]
	v_lshl_add_u64 v[130:131], s[8:9], 0, v[130:131]
	v_lshl_add_u64 v[130:131], v[130:131], 0, v[172:173]
	v_pk_mul_f32 v[132:133], v[124:125], v[16:17]
	v_pk_mul_f32 v[124:125], v[122:123], v[14:15]
	v_cvt_pk_bf16_f32 v122, v126, v127
	v_cvt_pk_bf16_f32 v123, v128, v129
	v_pk_mul_f32 v[112:113], v[112:113], v[12:13]
	v_cvt_pk_bf16_f32 v124, v124, v125
	v_cvt_pk_bf16_f32 v125, v132, v133
	global_store_dwordx4 v[130:131], v[122:125], off
	v_pk_mul_f32 v[110:111], v[110:111], v[10:11]
	v_pk_mul_f32 v[102:103], v[102:103], v[2:3]
	v_pk_mul_f32 v[122:123], v[116:117], v[8:9]
	v_pk_mul_f32 v[116:117], v[114:115], v[6:7]
	v_cvt_pk_bf16_f32 v114, v118, v119
	v_cvt_pk_bf16_f32 v115, v120, v121
	v_pk_mul_f32 v[104:105], v[104:105], v[4:5]
	v_cvt_pk_bf16_f32 v116, v116, v117
	v_cvt_pk_bf16_f32 v117, v122, v123
	global_store_dwordx4 v[130:131], v[114:117], off offset:256
	v_pk_mul_f32 v[96:97], v[96:97], v[12:13]
	v_pk_mul_f32 v[94:95], v[94:95], v[10:11]
	v_or_b32_e32 v114, 32, v168
	v_ashrrev_i32_e32 v115, 31, v114
	v_lshlrev_b64 v[114:115], 13, v[114:115]
	v_lshl_add_u64 v[114:115], s[8:9], 0, v[114:115]
	v_lshl_add_u64 v[114:115], v[114:115], 0, v[172:173]
	v_pk_mul_f32 v[116:117], v[108:109], v[16:17]
	v_pk_mul_f32 v[108:109], v[106:107], v[14:15]
	v_cvt_pk_bf16_f32 v106, v110, v111
	v_cvt_pk_bf16_f32 v107, v112, v113
	v_pk_mul_f32 v[88:89], v[88:89], v[4:5]
	v_cvt_pk_bf16_f32 v108, v108, v109
	v_cvt_pk_bf16_f32 v109, v116, v117
	global_store_dwordx4 v[114:115], v[106:109], off
	v_pk_mul_f32 v[86:87], v[86:87], v[2:3]
	v_pk_mul_f32 v[78:79], v[78:79], v[10:11]
	v_pk_mul_f32 v[106:107], v[100:101], v[8:9]
	v_pk_mul_f32 v[100:101], v[98:99], v[6:7]
	v_cvt_pk_bf16_f32 v98, v102, v103
	v_cvt_pk_bf16_f32 v99, v104, v105
	v_pk_mul_f32 v[80:81], v[80:81], v[12:13]
	v_cvt_pk_bf16_f32 v100, v100, v101
	v_cvt_pk_bf16_f32 v101, v106, v107
	global_store_dwordx4 v[114:115], v[98:101], off offset:256
	v_pk_mul_f32 v[72:73], v[72:73], v[4:5]
	v_pk_mul_f32 v[70:71], v[70:71], v[2:3]
	v_or_b32_e32 v98, 48, v168
	v_ashrrev_i32_e32 v99, 31, v98
	v_lshlrev_b64 v[98:99], 13, v[98:99]
	v_lshl_add_u64 v[98:99], s[8:9], 0, v[98:99]
	v_lshl_add_u64 v[98:99], v[98:99], 0, v[172:173]
	v_pk_mul_f32 v[100:101], v[92:93], v[16:17]
	v_pk_mul_f32 v[92:93], v[90:91], v[14:15]
	v_cvt_pk_bf16_f32 v90, v94, v95
	v_cvt_pk_bf16_f32 v91, v96, v97
	v_pk_mul_f32 v[66:67], v[66:67], v[10:11]
	v_cvt_pk_bf16_f32 v92, v92, v93
	v_cvt_pk_bf16_f32 v93, v100, v101
	global_store_dwordx4 v[98:99], v[90:93], off
	v_pk_mul_f32 v[56:57], v[56:57], v[4:5]
	v_pk_mul_f32 v[54:55], v[54:55], v[2:3]
	v_pk_mul_f32 v[90:91], v[84:85], v[8:9]
	v_pk_mul_f32 v[84:85], v[82:83], v[6:7]
	v_cvt_pk_bf16_f32 v82, v86, v87
	v_cvt_pk_bf16_f32 v83, v88, v89
	v_pk_mul_f32 v[50:51], v[50:51], v[10:11]
	v_cvt_pk_bf16_f32 v84, v84, v85
	v_cvt_pk_bf16_f32 v85, v90, v91
	global_store_dwordx4 v[98:99], v[82:85], off offset:256
	v_pk_mul_f32 v[10:11], v[34:35], v[10:11]
	v_pk_mul_f32 v[40:41], v[40:41], v[4:5]
	v_pk_mul_f32 v[84:85], v[76:77], v[16:17]
	v_pk_mul_f32 v[76:77], v[74:75], v[14:15]
	v_cvt_pk_bf16_f32 v74, v78, v79
	v_add_co_u32_e64 v78, s[6:7], s55, v162
	v_cvt_pk_bf16_f32 v75, v80, v81
	v_cvt_pk_bf16_f32 v76, v76, v77
	v_cvt_pk_bf16_f32 v77, v84, v85
	v_lshl_add_u64 v[82:83], v[162:163], 0, s[12:13]
	s_nop 0
	v_addc_co_u32_e64 v79, s[6:7], 0, v163, s[6:7]
	global_store_dwordx4 v[78:79], v[74:77], off
	v_pk_mul_f32 v[38:39], v[38:39], v[2:3]
	v_pk_mul_f32 v[4:5], v[24:25], v[4:5]
	v_pk_mul_f32 v[74:75], v[64:65], v[8:9]
	v_pk_mul_f32 v[64:65], v[62:63], v[6:7]
	v_cvt_pk_bf16_f32 v62, v70, v71
	v_cvt_pk_bf16_f32 v63, v72, v73
	v_pk_mul_f32 v[2:3], v[22:23], v[2:3]
	v_cvt_pk_bf16_f32 v64, v64, v65
	v_cvt_pk_bf16_f32 v65, v74, v75
	global_store_dwordx4 v[82:83], v[62:65], off offset:256
	s_and_b64 vcc, vcc, exec
	v_readlane_b32 s72, v254, 51
	v_pk_mul_f32 v[64:65], v[68:69], v[12:13]
	v_pk_mul_f32 v[68:69], v[60:61], v[16:17]
	v_pk_mul_f32 v[60:61], v[58:59], v[14:15]
	v_cvt_pk_bf16_f32 v58, v66, v67
	v_cvt_pk_bf16_f32 v59, v64, v65
	v_add_co_u32_e64 v64, s[6:7], s56, v162
	v_cvt_pk_bf16_f32 v60, v60, v61
	v_cvt_pk_bf16_f32 v61, v68, v69
	v_lshl_add_u64 v[62:63], v[162:163], 0, s[14:15]
	s_nop 0
	v_addc_co_u32_e64 v65, s[6:7], 0, v163, s[6:7]
	global_store_dwordx4 v[64:65], v[58:61], off
	v_readlane_b32 s73, v254, 52
	s_nop 0
	v_pk_mul_f32 v[58:59], v[48:49], v[8:9]
	v_pk_mul_f32 v[48:49], v[46:47], v[6:7]
	v_cvt_pk_bf16_f32 v46, v54, v55
	v_cvt_pk_bf16_f32 v47, v56, v57
	s_nop 0
	v_cvt_pk_bf16_f32 v48, v48, v49
	v_cvt_pk_bf16_f32 v49, v58, v59
	global_store_dwordx4 v[62:63], v[46:49], off offset:256
	s_nop 1
	v_pk_mul_f32 v[48:49], v[52:53], v[12:13]
	v_pk_mul_f32 v[52:53], v[44:45], v[16:17]
	v_pk_mul_f32 v[44:45], v[42:43], v[14:15]
	v_cvt_pk_bf16_f32 v42, v50, v51
	v_cvt_pk_bf16_f32 v43, v48, v49
	v_add_co_u32_e64 v48, s[6:7], s57, v162
	v_lshl_add_u64 v[46:47], v[162:163], 0, s[16:17]
	s_nop 0
	v_addc_co_u32_e64 v49, s[6:7], 0, v163, s[6:7]
	v_cvt_pk_bf16_f32 v44, v44, v45
	v_cvt_pk_bf16_f32 v45, v52, v53
	global_store_dwordx4 v[48:49], v[42:45], off
	v_pk_mul_f32 v[12:13], v[36:37], v[12:13]
	v_pk_mul_f32 v[14:15], v[26:27], v[14:15]
	v_pk_mul_f32 v[42:43], v[32:33], v[8:9]
	v_pk_mul_f32 v[32:33], v[30:31], v[6:7]
	v_cvt_pk_bf16_f32 v30, v38, v39
	v_cvt_pk_bf16_f32 v31, v40, v41
	v_pk_mul_f32 v[16:17], v[28:29], v[16:17]
	v_cvt_pk_bf16_f32 v32, v32, v33
	v_cvt_pk_bf16_f32 v33, v42, v43
	global_store_dwordx4 v[46:47], v[30:33], off offset:256
	v_cvt_pk_bf16_f32 v10, v10, v11
	v_cvt_pk_bf16_f32 v11, v12, v13
	v_cvt_pk_bf16_f32 v12, v14, v15
	v_add_co_u32_e64 v14, s[6:7], s58, v162
	s_nop 0
	v_lshl_add_u64 v[30:31], v[162:163], 0, s[18:19]
	v_addc_co_u32_e64 v15, s[6:7], 0, v163, s[6:7]
	v_cvt_pk_bf16_f32 v13, v16, v17
	global_store_dwordx4 v[14:15], v[10:13], off
	v_pk_mul_f32 v[8:9], v[20:21], v[8:9]
	v_pk_mul_f32 v[6:7], v[18:19], v[6:7]
	v_cvt_pk_bf16_f32 v2, v2, v3
	v_cvt_pk_bf16_f32 v3, v4, v5
	s_mov_b64 s[6:7], -1
	v_cvt_pk_bf16_f32 v4, v6, v7
	v_cvt_pk_bf16_f32 v5, v8, v9
	global_store_dwordx4 v[30:31], v[2:5], off offset:256
	v_readfirstlane_b32 s99, v0
	s_cmpk_gt_u32 s99, 0xff
	s_cbranch_scc0 .Lz1_1106
	s_barrier
.Lz1_1106:
	s_cbranch_vccz .LBB0_1098
	s_lshl_b32 s6, s20, 8
	s_or_b32 s6, s21, s6
	v_or_b32_e32 v2, s6, v167
	s_lshr_b32 s6, s23, 27
	s_add_i32 s6, s22, s6
	s_ashr_i32 s6, s6, 5
	s_mul_i32 s6, s6, 6
	s_ashr_i32 s7, s6, 31
	s_lshl_b64 s[6:7], s[6:7], 13
	s_add_u32 s6, s42, s6
	v_ashrrev_i32_e32 v3, 31, v2
	s_addc_u32 s7, s43, s7
	v_lshl_add_u64 v[6:7], v[2:3], 2, s[6:7]
	v_lshl_add_u64 v[2:3], v[6:7], 0, 16
	global_load_dwordx4 v[10:13], v[6:7], off
	global_load_dwordx4 v[14:17], v[2:3], off
	v_lshl_add_u64 v[2:3], v[6:7], 0, s[2:3]
	v_lshl_add_u64 v[6:7], v[6:7], 0, s[4:5]
	s_mov_b64 s[6:7], 0
	global_load_dwordx4 v[2:5], v[2:3], off
	global_load_dwordx4 v[6:9], v[6:7], off
	s_branch .LBB0_1098

.LBB0_1442:
	s_add_u32 s48, s96, s46
	s_addc_u32 s49, s97, s47
	s_add_u32 s50, s48, 0x32370200
	ds_read_b128 v[188:191], v176
	ds_read_b128 v[192:195], v176 offset:1024
	ds_read_b128 v[196:199], v176 offset:2048
	ds_read_b128 v[200:203], v176 offset:3072
	s_addc_u32 s51, s49, 0
	s_add_u32 s81, s78, s46
	s_addc_u32 s82, s79, s47
	s_cmpk_eq_i32 s46, 0x600
	s_cselect_b64 vcc, -1, 0
	s_and_b64 s[48:49], vcc, exec
	v_cndmask_b32_e32 v166, v184, v180, vcc
	s_cselect_b32 s51, s11, s51
	s_cselect_b32 s50, s10, s50
	v_cndmask_b32_e32 v252, v172, v182, vcc
	v_cndmask_b32_e32 v169, v168, v181, vcc
	v_cndmask_b32_e32 v171, v170, v183, vcc
	s_cselect_b32 s49, s39, s82
	s_cselect_b32 s48, s41, s81
	s_mov_b32 m0, s45
	v_lshl_add_u64 v[6:7], v[4:5], 0, s[46:47]
	ds_read_b128 v[10:13], v177
	ds_read_b128 v[14:17], v177 offset:1024
	ds_read_b128 v[204:207], v177 offset:2048
	ds_read_b128 v[208:211], v177 offset:3072
	ds_read_b128 v[212:215], v177 offset:4096
	ds_read_b128 v[216:219], v177 offset:5120
	ds_read_b128 v[220:223], v177 offset:6144
	ds_read_b128 v[224:227], v177 offset:7168
	global_load_lds_dwordx4 v[6:7], off
	v_lshl_add_u64 v[6:7], v[2:3], 0, s[46:47]
	s_mov_b32 m0, s69
	s_nop 0
	global_load_lds_dwordx4 v[6:7], off
	ds_read_b128 v[228:231], v178
	ds_read_b128 v[232:235], v178 offset:1024
	ds_read_b128 v[236:239], v178 offset:2048
	ds_read_b128 v[240:243], v178 offset:3072
	s_waitcnt vmcnt(8) lgkmcnt(0)
	s_barrier
	s_setprio 1
	v_mfma_f32_16x16x128_f8f6f4 v[154:157], v[188:195], v[10:17], v[154:157]
	v_mfma_f32_16x16x128_f8f6f4 v[146:149], v[196:203], v[10:17], v[146:149]
	v_mfma_f32_16x16x128_f8f6f4 v[138:141], v[188:195], v[204:211], v[138:141]
	v_mfma_f32_16x16x128_f8f6f4 v[130:133], v[196:203], v[204:211], v[130:133]
	v_mfma_f32_16x16x128_f8f6f4 v[122:125], v[188:195], v[212:219], v[122:125]
	v_mfma_f32_16x16x128_f8f6f4 v[114:117], v[196:203], v[212:219], v[114:117]
	v_mfma_f32_16x16x128_f8f6f4 v[106:109], v[188:195], v[220:227], v[106:109]
	v_mfma_f32_16x16x128_f8f6f4 v[90:93], v[196:203], v[220:227], v[90:93]
	v_mfma_f32_16x16x128_f8f6f4 v[158:161], v[228:235], v[10:17], v[158:161]
	v_mfma_f32_16x16x128_f8f6f4 v[150:153], v[236:243], v[10:17], v[150:153]
	v_mfma_f32_16x16x128_f8f6f4 v[142:145], v[228:235], v[204:211], v[142:145]
	v_mfma_f32_16x16x128_f8f6f4 v[134:137], v[236:243], v[204:211], v[134:137]
	v_mfma_f32_16x16x128_f8f6f4 v[126:129], v[228:235], v[212:219], v[126:129]
	v_mfma_f32_16x16x128_f8f6f4 v[118:121], v[236:243], v[212:219], v[118:121]
	v_mfma_f32_16x16x128_f8f6f4 v[110:113], v[228:235], v[220:227], v[110:113]
	v_mfma_f32_16x16x128_f8f6f4 v[98:101], v[236:243], v[220:227], v[98:101]
	s_setprio 0
	s_barrier
	ds_read_b128 v[204:207], v177 offset:16384
	ds_read_b128 v[208:211], v177 offset:17408
	ds_read_b128 v[212:215], v177 offset:18432
	ds_read_b128 v[216:219], v177 offset:19456
	ds_read_b128 v[220:223], v177 offset:20480
	ds_read_b128 v[224:227], v177 offset:21504
	ds_read_b128 v[244:247], v177 offset:22528
	ds_read_b128 v[248:251], v177 offset:23552
	s_mov_b32 m0, s70
	v_lshl_add_u64 v[6:7], s[48:49], 0, v[162:163]
	global_load_lds_dwordx4 v[6:7], off
	v_lshl_add_u64 v[8:9], s[48:49], 0, v[164:165]
	s_mov_b32 m0, s71
	s_nop 0
	global_load_lds_dwordx4 v[8:9], off
	s_mov_b32 m0, s55
	s_nop 0
	global_load_lds_dwordx4 v166, s[50:51]
	s_mov_b32 m0, s56
	v_mov_b32_e32 v253, v167
	global_load_lds_dwordx4 v252, s[50:51]
	s_add_u32 s82, s48, 0x40000
	s_addc_u32 s83, s49, 0
	s_mov_b32 m0, s72
	v_lshl_add_u64 v[14:15], s[82:83], 0, v[162:163]
	global_load_lds_dwordx4 v[14:15], off
	v_lshl_add_u64 v[14:15], s[82:83], 0, v[164:165]
	s_mov_b32 m0, s73
	s_nop 0
	global_load_lds_dwordx4 v[14:15], off
	s_waitcnt vmcnt(8) lgkmcnt(0)
	s_barrier
	v_lshl_add_u64 v[12:13], s[50:51], 0, v[166:167]
	v_lshl_add_u64 v[10:11], s[50:51], 0, v[252:253]
	s_setprio 1
	v_mfma_f32_16x16x128_f8f6f4 v[94:97], v[188:195], v[204:211], v[94:97]
	v_mfma_f32_16x16x128_f8f6f4 v[82:85], v[196:203], v[204:211], v[82:85]
	v_mfma_f32_16x16x128_f8f6f4 v[74:77], v[188:195], v[212:219], v[74:77]
	v_mfma_f32_16x16x128_f8f6f4 v[66:69], v[196:203], v[212:219], v[66:69]
	v_mfma_f32_16x16x128_f8f6f4 v[58:61], v[188:195], v[220:227], v[58:61]
	v_mfma_f32_16x16x128_f8f6f4 v[50:53], v[196:203], v[220:227], v[50:53]
	v_mfma_f32_16x16x128_f8f6f4 v[42:45], v[188:195], v[244:251], v[42:45]
	v_mfma_f32_16x16x128_f8f6f4 v[34:37], v[196:203], v[244:251], v[34:37]
	v_mfma_f32_16x16x128_f8f6f4 v[102:105], v[228:235], v[204:211], v[102:105]
	v_mfma_f32_16x16x128_f8f6f4 v[86:89], v[236:243], v[204:211], v[86:89]
	v_mfma_f32_16x16x128_f8f6f4 v[78:81], v[228:235], v[212:219], v[78:81]
	v_mfma_f32_16x16x128_f8f6f4 v[70:73], v[236:243], v[212:219], v[70:73]
	v_mfma_f32_16x16x128_f8f6f4 v[62:65], v[228:235], v[220:227], v[62:65]
	v_mfma_f32_16x16x128_f8f6f4 v[54:57], v[236:243], v[220:227], v[54:57]
	v_mfma_f32_16x16x128_f8f6f4 v[46:49], v[228:235], v[244:251], v[46:49]
	v_mfma_f32_16x16x128_f8f6f4 v[38:41], v[236:243], v[244:251], v[38:41]
	s_setprio 0
	s_barrier
	ds_read_b128 v[188:191], v185
	ds_read_b128 v[192:195], v185 offset:1024
	ds_read_b128 v[196:199], v185 offset:2048
	ds_read_b128 v[200:203], v185 offset:3072
	s_mov_b32 m0, s57
	ds_read_b128 v[204:207], v177 offset:32768
	ds_read_b128 v[208:211], v177 offset:33792
	ds_read_b128 v[212:215], v177 offset:34816
	ds_read_b128 v[216:219], v177 offset:35840
	ds_read_b128 v[220:223], v177 offset:36864
	ds_read_b128 v[224:227], v177 offset:37888
	ds_read_b128 v[228:231], v177 offset:38912
	ds_read_b128 v[232:235], v177 offset:39936
	global_load_lds_dwordx4 v169, s[50:51]
	s_mov_b32 m0, s58
	s_nop 0
	global_load_lds_dwordx4 v171, s[50:51]
	ds_read_b128 v[236:239], v186
	ds_read_b128 v[240:243], v186 offset:1024
	ds_read_b128 v[244:247], v186 offset:2048
	ds_read_b128 v[248:251], v186 offset:3072
	s_waitcnt vmcnt(8) lgkmcnt(0)
	s_barrier
	s_setprio 1
	v_mfma_f32_16x16x128_f8f6f4 v[154:157], v[188:195], v[204:211], v[154:157]
	v_mfma_f32_16x16x128_f8f6f4 v[146:149], v[196:203], v[204:211], v[146:149]
	v_mfma_f32_16x16x128_f8f6f4 v[138:141], v[188:195], v[212:219], v[138:141]
	v_mfma_f32_16x16x128_f8f6f4 v[130:133], v[196:203], v[212:219], v[130:133]
	v_mfma_f32_16x16x128_f8f6f4 v[122:125], v[188:195], v[220:227], v[122:125]
	v_mfma_f32_16x16x128_f8f6f4 v[114:117], v[196:203], v[220:227], v[114:117]
	v_mfma_f32_16x16x128_f8f6f4 v[106:109], v[188:195], v[228:235], v[106:109]
	v_mfma_f32_16x16x128_f8f6f4 v[90:93], v[196:203], v[228:235], v[90:93]
	v_mfma_f32_16x16x128_f8f6f4 v[158:161], v[236:243], v[204:211], v[158:161]
	v_mfma_f32_16x16x128_f8f6f4 v[150:153], v[244:251], v[204:211], v[150:153]
	v_mfma_f32_16x16x128_f8f6f4 v[142:145], v[236:243], v[212:219], v[142:145]
	v_mfma_f32_16x16x128_f8f6f4 v[134:137], v[244:251], v[212:219], v[134:137]
	v_mfma_f32_16x16x128_f8f6f4 v[126:129], v[236:243], v[220:227], v[126:129]
	v_mfma_f32_16x16x128_f8f6f4 v[118:121], v[244:251], v[220:227], v[118:121]
	v_mfma_f32_16x16x128_f8f6f4 v[110:113], v[236:243], v[228:235], v[110:113]
	v_mfma_f32_16x16x128_f8f6f4 v[98:101], v[244:251], v[228:235], v[98:101]
	s_setprio 0
	s_barrier
	ds_read_b128 v[204:207], v177 offset:49152
	ds_read_b128 v[208:211], v177 offset:50176
	ds_read_b128 v[212:215], v177 offset:51200
	ds_read_b128 v[216:219], v177 offset:52224
	ds_read_b128 v[220:223], v177 offset:53248
	ds_read_b128 v[224:227], v177 offset:54272
	ds_read_b128 v[228:231], v177 offset:55296
	ds_read_b128 v[232:235], v177 offset:56320
	s_mov_b32 m0, s74
	v_lshl_add_u64 v[6:7], v[6:7], 0, s[18:19]
	global_load_lds_dwordx4 v[6:7], off
	v_lshl_add_u64 v[6:7], v[8:9], 0, s[18:19]
	s_mov_b32 m0, s75
	s_nop 0
	global_load_lds_dwordx4 v[6:7], off
	s_mov_b32 m0, s60
	v_lshl_add_u64 v[6:7], v[12:13], 0, s[18:19]
	global_load_lds_dwordx4 v[6:7], off
	v_lshl_add_u64 v[6:7], v[10:11], 0, s[18:19]
	s_mov_b32 m0, s61
	s_nop 0
	global_load_lds_dwordx4 v[6:7], off
	s_add_u32 s48, s48, 0x40080
	s_addc_u32 s49, s49, 0
	s_mov_b32 m0, s76
	v_lshl_add_u64 v[6:7], s[48:49], 0, v[162:163]
	global_load_lds_dwordx4 v[6:7], off
	v_lshl_add_u64 v[6:7], s[48:49], 0, v[164:165]
	s_mov_b32 m0, s77
	s_nop 0
	global_load_lds_dwordx4 v[6:7], off
	s_waitcnt vmcnt(8) lgkmcnt(0)
	s_barrier
	s_setprio 1
	v_mfma_f32_16x16x128_f8f6f4 v[94:97], v[188:195], v[204:211], v[94:97]
	v_mfma_f32_16x16x128_f8f6f4 v[82:85], v[196:203], v[204:211], v[82:85]
	v_mfma_f32_16x16x128_f8f6f4 v[74:77], v[188:195], v[212:219], v[74:77]
	v_mfma_f32_16x16x128_f8f6f4 v[66:69], v[196:203], v[212:219], v[66:69]
	v_mfma_f32_16x16x128_f8f6f4 v[58:61], v[188:195], v[220:227], v[58:61]
	v_mfma_f32_16x16x128_f8f6f4 v[50:53], v[196:203], v[220:227], v[50:53]
	v_mfma_f32_16x16x128_f8f6f4 v[42:45], v[188:195], v[228:235], v[42:45]
	v_mfma_f32_16x16x128_f8f6f4 v[34:37], v[196:203], v[228:235], v[34:37]
	v_mfma_f32_16x16x128_f8f6f4 v[102:105], v[236:243], v[204:211], v[102:105]
	v_mfma_f32_16x16x128_f8f6f4 v[86:89], v[244:251], v[204:211], v[86:89]
	v_mfma_f32_16x16x128_f8f6f4 v[78:81], v[236:243], v[212:219], v[78:81]
	v_mfma_f32_16x16x128_f8f6f4 v[70:73], v[244:251], v[212:219], v[70:73]
	v_mfma_f32_16x16x128_f8f6f4 v[62:65], v[236:243], v[220:227], v[62:65]
	v_mfma_f32_16x16x128_f8f6f4 v[54:57], v[244:251], v[220:227], v[54:57]
	v_mfma_f32_16x16x128_f8f6f4 v[46:49], v[236:243], v[228:235], v[46:49]
	v_mfma_f32_16x16x128_f8f6f4 v[38:41], v[244:251], v[228:235], v[38:41]
	s_setprio 0
	s_add_i32 s80, s80, 2
	s_add_u32 s46, s46, 0x100
	s_addc_u32 s47, s47, 0
	s_cmp_gt_u32 s80, 13
	s_barrier
	s_cbranch_scc0 .LBB0_1442
	v_readfirstlane_b32 s99, v0
	s_cmpk_gt_u32 s99, 0xff
	s_cbranch_scc1 .Lz0_1442
	s_barrier
.Lz0_1442:
	v_mov_b32_e32 v2, v0
	s_nop 15
	s_nop 15
	s_waitcnt vmcnt(6)
	s_lshl_b32 s41, s68, 8
	v_readfirstlane_b32 s39, v2
	v_pk_fma_f32 v[10:11], v[154:155], s[30:31], v[30:31] op_sel_hi:[1,0,1]
	s_ashr_i32 s45, s39, 2
	v_min_f32_e32 v10, 0x40e00000, v10
	v_min_f32_e32 v11, 0x40e00000, v11
	s_andn2_b32 s45, s45, 63
	v_pk_mul_f32 v[12:13], v[10:11], s[34:35] op_sel_hi:[1,0]
	s_add_i32 s45, s45, s41
	v_exp_f32_e32 v12, v12
	v_exp_f32_e32 v13, v13
	v_and_or_b32 v6, v2, 15, s45
	v_lshrrev_b32_e32 v2, 1, v2
	v_and_b32_e32 v8, 24, v2
	v_pk_fma_f32 v[2:3], v[156:157], s[30:31], v[32:33] op_sel_hi:[1,0,1]
	v_pk_add_f32 v[12:13], v[12:13], 1.0 op_sel_hi:[1,0]
	v_min_f32_e32 v2, 0x40e00000, v2
	v_min_f32_e32 v3, 0x40e00000, v3
	v_pk_mul_f32 v[154:155], v[2:3], s[34:35] op_sel_hi:[1,0]
	v_rcp_f32_e32 v12, v12
	v_rcp_f32_e32 v13, v13
	v_exp_f32_e32 v154, v154
	v_exp_f32_e32 v155, v155
	v_pk_fma_f32 v[16:17], v[158:159], s[30:31], v[26:27] op_sel_hi:[1,0,1]
	v_pk_fma_f32 v[14:15], v[160:161], s[30:31], v[28:29] op_sel_hi:[1,0,1]
	v_med3_f32 v16, v16, s65, v179
	v_med3_f32 v17, v17, s65, v179
	v_pk_fma_f32 v[10:11], v[16:17], v[10:11], v[10:11]
	v_med3_f32 v14, v14, s65, v179
	v_med3_f32 v15, v15, s65, v179
	v_pk_mul_f32 v[10:11], v[10:11], v[12:13]
	v_pk_add_f32 v[12:13], v[154:155], 1.0 op_sel_hi:[1,0]
	v_pk_fma_f32 v[2:3], v[14:15], v[2:3], v[2:3]
	v_pk_fma_f32 v[14:15], v[146:147], s[30:31], v[22:23] op_sel_hi:[1,0,1]
	v_rcp_f32_e32 v12, v12
	v_rcp_f32_e32 v13, v13
	v_min_f32_e32 v14, 0x40e00000, v14
	v_min_f32_e32 v15, 0x40e00000, v15
	v_pk_mul_f32 v[146:147], v[14:15], s[34:35] op_sel_hi:[1,0]
	v_pk_mul_f32 v[2:3], v[2:3], v[12:13]
	v_exp_f32_e32 v146, v146
	v_exp_f32_e32 v147, v147
	v_pk_fma_f32 v[12:13], v[148:149], s[30:31], v[24:25] op_sel_hi:[1,0,1]
	v_pk_fma_f32 v[148:149], v[150:151], s[30:31], v[18:19] op_sel_hi:[1,0,1]
	v_min_f32_e32 v12, 0x40e00000, v12
	v_med3_f32 v148, v148, s65, v179
	v_med3_f32 v149, v149, s65, v179
	v_min_f32_e32 v13, 0x40e00000, v13
	v_pk_add_f32 v[146:147], v[146:147], 1.0 op_sel_hi:[1,0]
	v_pk_fma_f32 v[14:15], v[148:149], v[14:15], v[14:15]
	v_pk_mul_f32 v[148:149], v[12:13], s[34:35] op_sel_hi:[1,0]
	v_rcp_f32_e32 v146, v146
	v_rcp_f32_e32 v147, v147
	v_exp_f32_e32 v148, v148
	v_exp_f32_e32 v149, v149
	v_pk_fma_f32 v[16:17], v[152:153], s[30:31], v[20:21] op_sel_hi:[1,0,1]
	v_pk_mul_f32 v[14:15], v[14:15], v[146:147]
	v_med3_f32 v16, v16, s65, v179
	v_pk_add_f32 v[146:147], v[148:149], 1.0 op_sel_hi:[1,0]
	v_mov_b32_e32 v149, v167
	v_cvt_pk_fp8_f32 v149, v14, v15
	v_pk_fma_f32 v[14:15], v[138:139], s[30:31], v[30:31] op_sel_hi:[1,0,1]
	v_med3_f32 v17, v17, s65, v179
	v_mov_b32_e32 v148, v167
	v_min_f32_e32 v14, 0x40e00000, v14
	v_min_f32_e32 v15, 0x40e00000, v15
	v_cvt_pk_fp8_f32 v148, v10, v11
	v_pk_fma_f32 v[10:11], v[16:17], v[12:13], v[12:13]
	v_pk_mul_f32 v[16:17], v[14:15], s[34:35] op_sel_hi:[1,0]
	v_pk_fma_f32 v[12:13], v[140:141], s[30:31], v[32:33] op_sel_hi:[1,0,1]
	v_exp_f32_e32 v16, v16
	v_exp_f32_e32 v17, v17
	v_min_f32_e32 v12, 0x40e00000, v12
	v_min_f32_e32 v13, 0x40e00000, v13
	v_pk_fma_f32 v[140:141], v[142:143], s[30:31], v[26:27] op_sel_hi:[1,0,1]
	v_pk_add_f32 v[16:17], v[16:17], 1.0 op_sel_hi:[1,0]
	v_pk_mul_f32 v[142:143], v[12:13], s[34:35] op_sel_hi:[1,0]
	v_rcp_f32_e32 v16, v16
	v_rcp_f32_e32 v17, v17
	v_exp_f32_e32 v142, v142
	v_exp_f32_e32 v143, v143
	v_med3_f32 v140, v140, s65, v179
	v_med3_f32 v141, v141, s65, v179
	v_pk_fma_f32 v[14:15], v[140:141], v[14:15], v[14:15]
	v_pk_fma_f32 v[138:139], v[144:145], s[30:31], v[28:29] op_sel_hi:[1,0,1]
	v_pk_mul_f32 v[14:15], v[14:15], v[16:17]
	v_pk_add_f32 v[16:17], v[142:143], 1.0 op_sel_hi:[1,0]
	v_med3_f32 v138, v138, s65, v179
	v_rcp_f32_e32 v16, v16
	v_rcp_f32_e32 v17, v17
	v_med3_f32 v139, v139, s65, v179
	v_pk_fma_f32 v[130:131], v[130:131], s[30:31], v[22:23] op_sel_hi:[1,0,1]
	v_pk_fma_f32 v[12:13], v[138:139], v[12:13], v[12:13]
	v_min_f32_e32 v130, 0x40e00000, v130
	v_min_f32_e32 v131, 0x40e00000, v131
	v_pk_mul_f32 v[12:13], v[12:13], v[16:17]
	v_pk_fma_f32 v[16:17], v[132:133], s[30:31], v[24:25] op_sel_hi:[1,0,1]
	v_pk_fma_f32 v[132:133], v[136:137], s[30:31], v[20:21] op_sel_hi:[1,0,1]
	v_pk_mul_f32 v[136:137], v[130:131], s[34:35] op_sel_hi:[1,0]
	v_pk_fma_f32 v[134:135], v[134:135], s[30:31], v[18:19] op_sel_hi:[1,0,1]
	v_exp_f32_e32 v136, v136
	v_exp_f32_e32 v137, v137
	v_med3_f32 v134, v134, s65, v179
	v_med3_f32 v135, v135, s65, v179
	v_min_f32_e32 v16, 0x40e00000, v16
	v_min_f32_e32 v17, 0x40e00000, v17
	v_pk_fma_f32 v[130:131], v[134:135], v[130:131], v[130:131]
	v_pk_mul_f32 v[134:135], v[16:17], s[34:35] op_sel_hi:[1,0]
	v_pk_add_f32 v[136:137], v[136:137], 1.0 op_sel_hi:[1,0]
	v_exp_f32_e32 v134, v134
	v_exp_f32_e32 v135, v135
	v_rcp_f32_e32 v136, v136
	v_rcp_f32_e32 v137, v137
	v_med3_f32 v132, v132, s65, v179
	v_pk_add_f32 v[134:135], v[134:135], 1.0 op_sel_hi:[1,0]
	v_med3_f32 v133, v133, s65, v179
	v_pk_mul_f32 v[130:131], v[130:131], v[136:137]
	v_rcp_f32_e32 v134, v134
	v_rcp_f32_e32 v135, v135
	v_mov_b32_e32 v137, v167
	v_cvt_pk_fp8_f32 v137, v130, v131
	v_mov_b32_e32 v136, v167
	v_cvt_pk_fp8_f32 v136, v14, v15
	v_pk_fma_f32 v[14:15], v[132:133], v[16:17], v[16:17]
	v_pk_fma_f32 v[114:115], v[114:115], s[30:31], v[22:23] op_sel_hi:[1,0,1]
	v_pk_mul_f32 v[14:15], v[14:15], v[134:135]
	v_cvt_pk_fp8_f32 v136, v12, v13 op_sel:[0,0,1]
	v_cvt_pk_fp8_f32 v137, v14, v15 op_sel:[0,0,1]
	v_pk_fma_f32 v[14:15], v[122:123], s[30:31], v[30:31] op_sel_hi:[1,0,1]
	v_pk_fma_f32 v[12:13], v[124:125], s[30:31], v[32:33] op_sel_hi:[1,0,1]
	v_min_f32_e32 v14, 0x40e00000, v14
	v_min_f32_e32 v15, 0x40e00000, v15
	v_pk_mul_f32 v[16:17], v[14:15], s[34:35] op_sel_hi:[1,0]
	v_min_f32_e32 v12, 0x40e00000, v12
	v_exp_f32_e32 v16, v16
	v_exp_f32_e32 v17, v17
	v_min_f32_e32 v13, 0x40e00000, v13
	v_pk_fma_f32 v[124:125], v[126:127], s[30:31], v[26:27] op_sel_hi:[1,0,1]
	v_pk_mul_f32 v[126:127], v[12:13], s[34:35] op_sel_hi:[1,0]
	v_pk_add_f32 v[16:17], v[16:17], 1.0 op_sel_hi:[1,0]
	v_exp_f32_e32 v126, v126
	v_rcp_f32_e32 v16, v16
	v_rcp_f32_e32 v17, v17
	v_exp_f32_e32 v127, v127
	v_med3_f32 v124, v124, s65, v179
	v_med3_f32 v125, v125, s65, v179
	v_pk_fma_f32 v[14:15], v[124:125], v[14:15], v[14:15]
	v_pk_fma_f32 v[122:123], v[128:129], s[30:31], v[28:29] op_sel_hi:[1,0,1]
	v_pk_mul_f32 v[14:15], v[14:15], v[16:17]
	v_pk_add_f32 v[16:17], v[126:127], 1.0 op_sel_hi:[1,0]
	v_med3_f32 v122, v122, s65, v179
	v_rcp_f32_e32 v16, v16
	v_rcp_f32_e32 v17, v17
	v_med3_f32 v123, v123, s65, v179
	v_pk_fma_f32 v[12:13], v[122:123], v[12:13], v[12:13]
	v_min_f32_e32 v114, 0x40e00000, v114
	v_min_f32_e32 v115, 0x40e00000, v115
	v_pk_mul_f32 v[12:13], v[12:13], v[16:17]
	v_pk_fma_f32 v[16:17], v[116:117], s[30:31], v[24:25] op_sel_hi:[1,0,1]
	v_pk_fma_f32 v[116:117], v[120:121], s[30:31], v[20:21] op_sel_hi:[1,0,1]
	v_pk_mul_f32 v[120:121], v[114:115], s[34:35] op_sel_hi:[1,0]
	v_pk_fma_f32 v[118:119], v[118:119], s[30:31], v[18:19] op_sel_hi:[1,0,1]
	v_exp_f32_e32 v120, v120
	v_exp_f32_e32 v121, v121
	v_med3_f32 v118, v118, s65, v179
	v_med3_f32 v119, v119, s65, v179
	v_min_f32_e32 v16, 0x40e00000, v16
	v_min_f32_e32 v17, 0x40e00000, v17
	v_rcp_f32_e32 v146, v146
	v_rcp_f32_e32 v147, v147
	v_pk_add_f32 v[120:121], v[120:121], 1.0 op_sel_hi:[1,0]
	v_pk_fma_f32 v[114:115], v[118:119], v[114:115], v[114:115]
	v_pk_mul_f32 v[118:119], v[16:17], s[34:35] op_sel_hi:[1,0]
	v_rcp_f32_e32 v120, v120
	v_rcp_f32_e32 v121, v121
	v_exp_f32_e32 v118, v118
	v_exp_f32_e32 v119, v119
	s_lshr_b32 s39, s39, 1
	v_pk_mul_f32 v[10:11], v[10:11], v[146:147]
	s_lshl_b32 s41, s44, 7
	s_and_b32 s39, s39, 0x60
	v_cvt_pk_fp8_f32 v149, v10, v11 op_sel:[0,0,1]
	v_or_b32_e32 v10, 16, v6
	v_pk_mul_f32 v[114:115], v[114:115], v[120:121]
	v_pk_add_f32 v[118:119], v[118:119], 1.0 op_sel_hi:[1,0]
	v_mov_b32_e32 v120, v167
	s_or_b32 s41, s39, s41
	v_ashrrev_i32_e32 v11, 31, v10
	v_rcp_f32_e32 v118, v118
	v_rcp_f32_e32 v119, v119
	v_cvt_pk_fp8_f32 v120, v14, v15
	v_mov_b32_e32 v121, v167
	v_or_b32_e32 v4, s41, v8
	v_lshlrev_b64 v[10:11], 11, v[10:11]
	v_cvt_pk_fp8_f32 v121, v114, v115
	v_ashrrev_i32_e32 v5, 31, v4
	v_lshl_add_u64 v[10:11], s[16:17], 0, v[10:11]
	v_med3_f32 v116, v116, s65, v179
	v_med3_f32 v117, v117, s65, v179
	v_lshl_add_u64 v[10:11], v[10:11], 0, v[4:5]
	v_pk_fma_f32 v[14:15], v[116:117], v[16:17], v[16:17]
	global_store_dwordx2 v[10:11], v[136:137], off
	v_or_b32_e32 v10, 32, v6
	v_pk_mul_f32 v[14:15], v[14:15], v[118:119]
	v_cvt_pk_fp8_f32 v120, v12, v13 op_sel:[0,0,1]
	v_pk_fma_f32 v[12:13], v[106:107], s[30:31], v[30:31] op_sel_hi:[1,0,1]
	v_ashrrev_i32_e32 v11, 31, v10
	v_cvt_pk_fp8_f32 v121, v14, v15 op_sel:[0,0,1]
	v_min_f32_e32 v12, 0x40e00000, v12
	v_min_f32_e32 v13, 0x40e00000, v13
	v_lshlrev_b64 v[10:11], 11, v[10:11]
	v_pk_mul_f32 v[14:15], v[12:13], s[34:35] op_sel_hi:[1,0]
	v_lshl_add_u64 v[10:11], s[16:17], 0, v[10:11]
	v_exp_f32_e32 v14, v14
	v_exp_f32_e32 v15, v15
	v_lshl_add_u64 v[10:11], v[10:11], 0, v[4:5]
	global_store_dwordx2 v[10:11], v[120:121], off
	v_pk_fma_f32 v[10:11], v[108:109], s[30:31], v[32:33] op_sel_hi:[1,0,1]
	v_pk_add_f32 v[14:15], v[14:15], 1.0 op_sel_hi:[1,0]
	v_min_f32_e32 v10, 0x40e00000, v10
	v_min_f32_e32 v11, 0x40e00000, v11
	v_pk_mul_f32 v[108:109], v[10:11], s[34:35] op_sel_hi:[1,0]
	v_rcp_f32_e32 v14, v14
	v_rcp_f32_e32 v15, v15
	v_exp_f32_e32 v108, v108
	v_exp_f32_e32 v109, v109
	v_pk_fma_f32 v[106:107], v[110:111], s[30:31], v[26:27] op_sel_hi:[1,0,1]
	v_pk_fma_f32 v[16:17], v[112:113], s[30:31], v[28:29] op_sel_hi:[1,0,1]
	v_med3_f32 v106, v106, s65, v179
	v_med3_f32 v107, v107, s65, v179
	v_pk_fma_f32 v[12:13], v[106:107], v[12:13], v[12:13]
	v_med3_f32 v16, v16, s65, v179
	v_pk_mul_f32 v[12:13], v[12:13], v[14:15]
	v_pk_add_f32 v[14:15], v[108:109], 1.0 op_sel_hi:[1,0]
	v_med3_f32 v17, v17, s65, v179
	v_rcp_f32_e32 v14, v14
	v_rcp_f32_e32 v15, v15
	v_pk_fma_f32 v[10:11], v[16:17], v[10:11], v[10:11]
	v_pk_fma_f32 v[16:17], v[90:91], s[30:31], v[22:23] op_sel_hi:[1,0,1]
	v_pk_fma_f32 v[98:99], v[98:99], s[30:31], v[18:19] op_sel_hi:[1,0,1]
	v_min_f32_e32 v16, 0x40e00000, v16
	v_min_f32_e32 v17, 0x40e00000, v17
	v_pk_mul_f32 v[10:11], v[10:11], v[14:15]
	v_pk_fma_f32 v[14:15], v[92:93], s[30:31], v[24:25] op_sel_hi:[1,0,1]
	v_pk_mul_f32 v[92:93], v[16:17], s[34:35] op_sel_hi:[1,0]
	v_med3_f32 v98, v98, s65, v179
	v_exp_f32_e32 v92, v92
	v_exp_f32_e32 v93, v93
	v_med3_f32 v99, v99, s65, v179
	v_min_f32_e32 v14, 0x40e00000, v14
	v_min_f32_e32 v15, 0x40e00000, v15
	v_pk_add_f32 v[92:93], v[92:93], 1.0 op_sel_hi:[1,0]
	v_pk_fma_f32 v[16:17], v[98:99], v[16:17], v[16:17]
	v_pk_mul_f32 v[98:99], v[14:15], s[34:35] op_sel_hi:[1,0]
	v_rcp_f32_e32 v92, v92
	v_rcp_f32_e32 v93, v93
	v_exp_f32_e32 v98, v98
	v_exp_f32_e32 v99, v99
	v_ashrrev_i32_e32 v7, 31, v6
	v_pk_mul_f32 v[16:17], v[16:17], v[92:93]
	v_cvt_pk_fp8_f32 v148, v2, v3 op_sel:[0,0,1]
	v_pk_add_f32 v[92:93], v[98:99], 1.0 op_sel_hi:[1,0]
	v_lshlrev_b64 v[2:3], 11, v[6:7]
	v_or_b32_e32 v6, 48, v6
	v_rcp_f32_e32 v92, v92
	v_rcp_f32_e32 v93, v93
	v_mov_b32_e32 v98, v167
	v_mov_b32_e32 v99, v167
	v_ashrrev_i32_e32 v7, 31, v6
	v_pk_fma_f32 v[90:91], v[100:101], s[30:31], v[20:21] op_sel_hi:[1,0,1]
	v_cvt_pk_fp8_f32 v98, v12, v13
	v_cvt_pk_fp8_f32 v99, v16, v17
	v_med3_f32 v90, v90, s65, v179
	v_med3_f32 v91, v91, s65, v179
	v_lshlrev_b64 v[6:7], 11, v[6:7]
	v_lshl_add_u64 v[2:3], s[16:17], 0, v[2:3]
	v_pk_fma_f32 v[12:13], v[90:91], v[14:15], v[14:15]
	v_lshl_add_u64 v[6:7], s[16:17], 0, v[6:7]
	v_lshl_add_u64 v[2:3], v[2:3], 0, v[4:5]
	v_pk_mul_f32 v[12:13], v[12:13], v[92:93]
	v_lshl_add_u64 v[4:5], v[6:7], 0, v[4:5]
	v_pk_fma_f32 v[6:7], v[94:95], s[30:31], v[30:31] op_sel_hi:[1,0,1]
	v_cvt_pk_fp8_f32 v98, v10, v11 op_sel:[0,0,1]
	v_cvt_pk_fp8_f32 v99, v12, v13 op_sel:[0,0,1]
	v_min_f32_e32 v6, 0x40e00000, v6
	v_min_f32_e32 v7, 0x40e00000, v7
	v_pk_mul_f32 v[10:11], v[6:7], s[34:35] op_sel_hi:[1,0]
	global_store_dwordx2 v[4:5], v[98:99], off
	v_exp_f32_e32 v10, v10
	v_exp_f32_e32 v11, v11
	v_pk_fma_f32 v[4:5], v[96:97], s[30:31], v[32:33] op_sel_hi:[1,0,1]
	v_pk_fma_f32 v[14:15], v[102:103], s[30:31], v[26:27] op_sel_hi:[1,0,1]
	v_min_f32_e32 v4, 0x40e00000, v4
	v_min_f32_e32 v5, 0x40e00000, v5
	v_pk_add_f32 v[10:11], v[10:11], 1.0 op_sel_hi:[1,0]
	v_pk_mul_f32 v[16:17], v[4:5], s[34:35] op_sel_hi:[1,0]
	v_rcp_f32_e32 v10, v10
	v_rcp_f32_e32 v11, v11
	v_exp_f32_e32 v16, v16
	v_exp_f32_e32 v17, v17
	v_pk_fma_f32 v[12:13], v[104:105], s[30:31], v[28:29] op_sel_hi:[1,0,1]
	v_med3_f32 v14, v14, s65, v179
	v_med3_f32 v15, v15, s65, v179
	v_pk_fma_f32 v[6:7], v[14:15], v[6:7], v[6:7]
	v_med3_f32 v12, v12, s65, v179
	v_med3_f32 v13, v13, s65, v179
	v_pk_mul_f32 v[6:7], v[6:7], v[10:11]
	v_pk_add_f32 v[10:11], v[16:17], 1.0 op_sel_hi:[1,0]
	v_pk_fma_f32 v[4:5], v[12:13], v[4:5], v[4:5]
	v_pk_fma_f32 v[12:13], v[82:83], s[30:31], v[22:23] op_sel_hi:[1,0,1]
	v_rcp_f32_e32 v10, v10
	v_rcp_f32_e32 v11, v11
	v_min_f32_e32 v12, 0x40e00000, v12
	v_min_f32_e32 v13, 0x40e00000, v13
	v_pk_mul_f32 v[16:17], v[12:13], s[34:35] op_sel_hi:[1,0]
	v_pk_mul_f32 v[4:5], v[4:5], v[10:11]
	v_exp_f32_e32 v16, v16
	v_exp_f32_e32 v17, v17
	v_pk_fma_f32 v[10:11], v[84:85], s[30:31], v[24:25] op_sel_hi:[1,0,1]
	v_pk_fma_f32 v[82:83], v[86:87], s[30:31], v[18:19] op_sel_hi:[1,0,1]
	v_min_f32_e32 v10, 0x40e00000, v10
	v_med3_f32 v82, v82, s65, v179
	v_med3_f32 v83, v83, s65, v179
	v_min_f32_e32 v11, 0x40e00000, v11
	v_pk_add_f32 v[16:17], v[16:17], 1.0 op_sel_hi:[1,0]
	v_pk_fma_f32 v[12:13], v[82:83], v[12:13], v[12:13]
	v_pk_mul_f32 v[82:83], v[10:11], s[34:35] op_sel_hi:[1,0]
	v_rcp_f32_e32 v16, v16
	v_rcp_f32_e32 v17, v17
	v_exp_f32_e32 v82, v82
	v_exp_f32_e32 v83, v83
	v_pk_fma_f32 v[14:15], v[88:89], s[30:31], v[20:21] op_sel_hi:[1,0,1]
	v_pk_mul_f32 v[12:13], v[12:13], v[16:17]
	v_med3_f32 v14, v14, s65, v179
	v_pk_add_f32 v[16:17], v[82:83], 1.0 op_sel_hi:[1,0]
	v_mov_b32_e32 v83, v167
	v_rcp_f32_e32 v16, v16
	v_rcp_f32_e32 v17, v17
	v_mov_b32_e32 v82, v167
	v_cvt_pk_fp8_f32 v83, v12, v13
	v_med3_f32 v15, v15, s65, v179
	v_cvt_pk_fp8_f32 v82, v6, v7
	v_pk_fma_f32 v[6:7], v[14:15], v[10:11], v[10:11]
	s_mov_b32 s41, 0x40000
	v_pk_mul_f32 v[6:7], v[6:7], v[16:17]
	v_cvt_pk_fp8_f32 v82, v4, v5 op_sel:[0,0,1]
	v_cvt_pk_fp8_f32 v83, v6, v7 op_sel:[0,0,1]
	v_pk_fma_f32 v[6:7], v[74:75], s[30:31], v[30:31] op_sel_hi:[1,0,1]
	v_add_co_u32_e32 v4, vcc, s41, v2
	v_min_f32_e32 v6, 0x40e00000, v6
	v_min_f32_e32 v7, 0x40e00000, v7
	v_pk_mul_f32 v[10:11], v[6:7], s[34:35] op_sel_hi:[1,0]
	v_addc_co_u32_e32 v5, vcc, 0, v3, vcc
	v_exp_f32_e32 v10, v10
	v_exp_f32_e32 v11, v11
	global_store_dwordx2 v[4:5], v[82:83], off
	v_pk_fma_f32 v[4:5], v[76:77], s[30:31], v[32:33] op_sel_hi:[1,0,1]
	v_pk_fma_f32 v[14:15], v[78:79], s[30:31], v[26:27] op_sel_hi:[1,0,1]
	v_min_f32_e32 v4, 0x40e00000, v4
	v_min_f32_e32 v5, 0x40e00000, v5
	v_pk_add_f32 v[10:11], v[10:11], 1.0 op_sel_hi:[1,0]
	v_pk_mul_f32 v[16:17], v[4:5], s[34:35] op_sel_hi:[1,0]
	v_rcp_f32_e32 v10, v10
	v_rcp_f32_e32 v11, v11
	v_exp_f32_e32 v16, v16
	v_exp_f32_e32 v17, v17
	v_pk_fma_f32 v[12:13], v[80:81], s[30:31], v[28:29] op_sel_hi:[1,0,1]
	v_med3_f32 v14, v14, s65, v179
	v_med3_f32 v15, v15, s65, v179
	v_pk_fma_f32 v[6:7], v[14:15], v[6:7], v[6:7]
	v_med3_f32 v12, v12, s65, v179
	v_med3_f32 v13, v13, s65, v179
	v_pk_mul_f32 v[6:7], v[6:7], v[10:11]
	v_pk_add_f32 v[10:11], v[16:17], 1.0 op_sel_hi:[1,0]
	v_pk_fma_f32 v[4:5], v[12:13], v[4:5], v[4:5]
	v_pk_fma_f32 v[12:13], v[66:67], s[30:31], v[22:23] op_sel_hi:[1,0,1]
	v_rcp_f32_e32 v10, v10
	v_rcp_f32_e32 v11, v11
	v_min_f32_e32 v12, 0x40e00000, v12
	v_min_f32_e32 v13, 0x40e00000, v13
	v_pk_mul_f32 v[16:17], v[12:13], s[34:35] op_sel_hi:[1,0]
	v_pk_mul_f32 v[4:5], v[4:5], v[10:11]
	v_exp_f32_e32 v16, v16
	v_exp_f32_e32 v17, v17
	v_pk_fma_f32 v[10:11], v[68:69], s[30:31], v[24:25] op_sel_hi:[1,0,1]
	v_pk_fma_f32 v[66:67], v[70:71], s[30:31], v[18:19] op_sel_hi:[1,0,1]
	v_min_f32_e32 v10, 0x40e00000, v10
	v_med3_f32 v66, v66, s65, v179
	v_med3_f32 v67, v67, s65, v179
	v_min_f32_e32 v11, 0x40e00000, v11
	v_pk_add_f32 v[16:17], v[16:17], 1.0 op_sel_hi:[1,0]
	v_pk_fma_f32 v[12:13], v[66:67], v[12:13], v[12:13]
	v_pk_mul_f32 v[66:67], v[10:11], s[34:35] op_sel_hi:[1,0]
	v_rcp_f32_e32 v16, v16
	v_rcp_f32_e32 v17, v17
	v_exp_f32_e32 v66, v66
	v_exp_f32_e32 v67, v67
	v_pk_fma_f32 v[14:15], v[72:73], s[30:31], v[20:21] op_sel_hi:[1,0,1]
	v_pk_mul_f32 v[12:13], v[12:13], v[16:17]
	v_med3_f32 v14, v14, s65, v179
	v_pk_add_f32 v[16:17], v[66:67], 1.0 op_sel_hi:[1,0]
	v_mov_b32_e32 v67, v167
	v_rcp_f32_e32 v16, v16
	v_rcp_f32_e32 v17, v17
	v_mov_b32_e32 v66, v167
	v_cvt_pk_fp8_f32 v67, v12, v13
	v_med3_f32 v15, v15, s65, v179
	v_cvt_pk_fp8_f32 v66, v6, v7
	v_pk_fma_f32 v[6:7], v[14:15], v[10:11], v[10:11]
	s_mov_b32 s41, 0x48000
	v_pk_mul_f32 v[6:7], v[6:7], v[16:17]
	v_cvt_pk_fp8_f32 v66, v4, v5 op_sel:[0,0,1]
	v_cvt_pk_fp8_f32 v67, v6, v7 op_sel:[0,0,1]
	v_pk_fma_f32 v[6:7], v[58:59], s[30:31], v[30:31] op_sel_hi:[1,0,1]
	v_add_co_u32_e32 v4, vcc, s41, v2
	v_min_f32_e32 v6, 0x40e00000, v6
	v_min_f32_e32 v7, 0x40e00000, v7
	v_pk_mul_f32 v[10:11], v[6:7], s[34:35] op_sel_hi:[1,0]
	v_addc_co_u32_e32 v5, vcc, 0, v3, vcc
	v_exp_f32_e32 v10, v10
	v_exp_f32_e32 v11, v11
	global_store_dwordx2 v[4:5], v[66:67], off
	v_pk_fma_f32 v[4:5], v[60:61], s[30:31], v[32:33] op_sel_hi:[1,0,1]
	v_pk_fma_f32 v[14:15], v[62:63], s[30:31], v[26:27] op_sel_hi:[1,0,1]
	v_min_f32_e32 v4, 0x40e00000, v4
	v_min_f32_e32 v5, 0x40e00000, v5
	v_pk_add_f32 v[10:11], v[10:11], 1.0 op_sel_hi:[1,0]
	v_pk_mul_f32 v[16:17], v[4:5], s[34:35] op_sel_hi:[1,0]
	v_rcp_f32_e32 v10, v10
	v_rcp_f32_e32 v11, v11
	v_exp_f32_e32 v16, v16
	v_exp_f32_e32 v17, v17
	v_pk_fma_f32 v[12:13], v[64:65], s[30:31], v[28:29] op_sel_hi:[1,0,1]
	v_med3_f32 v14, v14, s65, v179
	v_med3_f32 v15, v15, s65, v179
	v_pk_fma_f32 v[6:7], v[14:15], v[6:7], v[6:7]
	v_med3_f32 v12, v12, s65, v179
	v_med3_f32 v13, v13, s65, v179
	v_pk_mul_f32 v[6:7], v[6:7], v[10:11]
	v_pk_add_f32 v[10:11], v[16:17], 1.0 op_sel_hi:[1,0]
	v_pk_fma_f32 v[4:5], v[12:13], v[4:5], v[4:5]
	v_pk_fma_f32 v[12:13], v[50:51], s[30:31], v[22:23] op_sel_hi:[1,0,1]
	v_rcp_f32_e32 v10, v10
	v_rcp_f32_e32 v11, v11
	v_min_f32_e32 v12, 0x40e00000, v12
	v_min_f32_e32 v13, 0x40e00000, v13
	v_pk_mul_f32 v[16:17], v[12:13], s[34:35] op_sel_hi:[1,0]
	v_pk_mul_f32 v[4:5], v[4:5], v[10:11]
	v_exp_f32_e32 v16, v16
	v_exp_f32_e32 v17, v17
	v_pk_fma_f32 v[10:11], v[52:53], s[30:31], v[24:25] op_sel_hi:[1,0,1]
	v_pk_fma_f32 v[50:51], v[54:55], s[30:31], v[18:19] op_sel_hi:[1,0,1]
	v_min_f32_e32 v10, 0x40e00000, v10
	v_med3_f32 v50, v50, s65, v179
	v_med3_f32 v51, v51, s65, v179
	v_min_f32_e32 v11, 0x40e00000, v11
	v_pk_add_f32 v[16:17], v[16:17], 1.0 op_sel_hi:[1,0]
	v_pk_fma_f32 v[12:13], v[50:51], v[12:13], v[12:13]
	v_pk_mul_f32 v[50:51], v[10:11], s[34:35] op_sel_hi:[1,0]
	v_rcp_f32_e32 v16, v16
	v_rcp_f32_e32 v17, v17
	v_exp_f32_e32 v50, v50
	v_exp_f32_e32 v51, v51
	v_pk_fma_f32 v[14:15], v[56:57], s[30:31], v[20:21] op_sel_hi:[1,0,1]
	v_pk_mul_f32 v[12:13], v[12:13], v[16:17]
	v_med3_f32 v14, v14, s65, v179
	v_pk_add_f32 v[16:17], v[50:51], 1.0 op_sel_hi:[1,0]
	v_mov_b32_e32 v51, v167
	v_rcp_f32_e32 v16, v16
	v_rcp_f32_e32 v17, v17
	v_mov_b32_e32 v50, v167
	v_cvt_pk_fp8_f32 v51, v12, v13
	v_med3_f32 v15, v15, s65, v179
	v_cvt_pk_fp8_f32 v50, v6, v7
	v_pk_fma_f32 v[6:7], v[14:15], v[10:11], v[10:11]
	s_mov_b32 s41, 0x50000
	v_pk_mul_f32 v[6:7], v[6:7], v[16:17]
	v_cvt_pk_fp8_f32 v50, v4, v5 op_sel:[0,0,1]
	v_cvt_pk_fp8_f32 v51, v6, v7 op_sel:[0,0,1]
	v_pk_fma_f32 v[6:7], v[42:43], s[30:31], v[30:31] op_sel_hi:[1,0,1]
	v_add_co_u32_e32 v4, vcc, s41, v2
	v_min_f32_e32 v6, 0x40e00000, v6
	v_min_f32_e32 v7, 0x40e00000, v7
	v_pk_mul_f32 v[10:11], v[6:7], s[34:35] op_sel_hi:[1,0]
	v_addc_co_u32_e32 v5, vcc, 0, v3, vcc
	v_exp_f32_e32 v10, v10
	v_exp_f32_e32 v11, v11
	global_store_dwordx2 v[4:5], v[50:51], off
	v_pk_fma_f32 v[4:5], v[44:45], s[30:31], v[32:33] op_sel_hi:[1,0,1]
	v_pk_fma_f32 v[14:15], v[46:47], s[30:31], v[26:27] op_sel_hi:[1,0,1]
	v_min_f32_e32 v4, 0x40e00000, v4
	v_min_f32_e32 v5, 0x40e00000, v5
	v_pk_add_f32 v[10:11], v[10:11], 1.0 op_sel_hi:[1,0]
	v_pk_mul_f32 v[16:17], v[4:5], s[34:35] op_sel_hi:[1,0]
	v_rcp_f32_e32 v10, v10
	v_rcp_f32_e32 v11, v11
	v_exp_f32_e32 v16, v16
	v_exp_f32_e32 v17, v17
	v_pk_fma_f32 v[12:13], v[48:49], s[30:31], v[28:29] op_sel_hi:[1,0,1]
	v_med3_f32 v14, v14, s65, v179
	v_med3_f32 v15, v15, s65, v179
	v_pk_fma_f32 v[6:7], v[14:15], v[6:7], v[6:7]
	v_med3_f32 v12, v12, s65, v179
	v_med3_f32 v13, v13, s65, v179
	v_pk_mul_f32 v[6:7], v[6:7], v[10:11]
	v_pk_add_f32 v[10:11], v[16:17], 1.0 op_sel_hi:[1,0]
	v_pk_fma_f32 v[4:5], v[12:13], v[4:5], v[4:5]
	v_pk_fma_f32 v[12:13], v[34:35], s[30:31], v[22:23] op_sel_hi:[1,0,1]
	v_rcp_f32_e32 v10, v10
	v_rcp_f32_e32 v11, v11
	v_min_f32_e32 v12, 0x40e00000, v12
	v_min_f32_e32 v13, 0x40e00000, v13
	v_pk_mul_f32 v[16:17], v[12:13], s[34:35] op_sel_hi:[1,0]
	v_pk_mul_f32 v[4:5], v[4:5], v[10:11]
	v_exp_f32_e32 v16, v16
	v_exp_f32_e32 v17, v17
	v_pk_fma_f32 v[10:11], v[36:37], s[30:31], v[24:25] op_sel_hi:[1,0,1]
	v_pk_fma_f32 v[18:19], v[38:39], s[30:31], v[18:19] op_sel_hi:[1,0,1]
	v_min_f32_e32 v10, 0x40e00000, v10
	v_med3_f32 v18, v18, s65, v179
	v_med3_f32 v19, v19, s65, v179
	v_min_f32_e32 v11, 0x40e00000, v11
	v_pk_add_f32 v[16:17], v[16:17], 1.0 op_sel_hi:[1,0]
	v_pk_fma_f32 v[12:13], v[18:19], v[12:13], v[12:13]
	v_pk_mul_f32 v[18:19], v[10:11], s[34:35] op_sel_hi:[1,0]
	v_rcp_f32_e32 v16, v16
	v_rcp_f32_e32 v17, v17
	v_exp_f32_e32 v18, v18
	v_exp_f32_e32 v19, v19
	v_pk_fma_f32 v[14:15], v[40:41], s[30:31], v[20:21] op_sel_hi:[1,0,1]
	v_pk_mul_f32 v[12:13], v[12:13], v[16:17]
	v_med3_f32 v14, v14, s65, v179
	v_pk_add_f32 v[16:17], v[18:19], 1.0 op_sel_hi:[1,0]
	v_mov_b32_e32 v18, v167
	v_rcp_f32_e32 v16, v16
	v_rcp_f32_e32 v17, v17
	v_mov_b32_e32 v19, v167
	v_cvt_pk_fp8_f32 v18, v6, v7
	v_cvt_pk_fp8_f32 v19, v12, v13
	v_med3_f32 v15, v15, s65, v179
	v_pk_fma_f32 v[6:7], v[14:15], v[10:11], v[10:11]
	v_cvt_pk_fp8_f32 v18, v4, v5 op_sel:[0,0,1]
	v_pk_mul_f32 v[6:7], v[6:7], v[16:17]
	global_store_dwordx2 v[2:3], v[148:149], off
	v_cvt_pk_fp8_f32 v19, v6, v7 op_sel:[0,0,1]
	v_add_co_u32_e32 v2, vcc, 0x58000, v2
	s_mov_b64 s[44:45], -1
	s_nop 0
	v_addc_co_u32_e32 v3, vcc, 0, v3, vcc
	s_and_b64 vcc, s[42:43], exec
	global_store_dwordx2 v[2:3], v[18:19], off
	v_readfirstlane_b32 s99, v0
	s_cmpk_gt_u32 s99, 0xff
	s_cbranch_scc0 .Lz1_1442
	s_barrier
.Lz1_1442:
	s_cbranch_vccz .LBB0_1434
	s_ashr_i32 s41, s40, 31
	s_lshl_b64 s[42:43], s[40:41], 14
	s_add_u32 s41, s88, s42
	s_addc_u32 s44, s89, s43
	s_lshl_b32 s42, s38, 7
	s_ashr_i32 s43, s42, 31
	s_lshl_b64 s[42:43], s[42:43], 2
	s_add_u32 s41, s41, s42
	s_addc_u32 s43, s44, s43
	s_lshl_b32 s39, s39, 2
	s_add_u32 s42, s41, s39
	s_addc_u32 s43, s43, 0
	v_lshlrev_b32_e32 v166, 2, v8
	v_lshl_add_u64 v[2:3], s[42:43], 0, v[166:167]
	v_lshl_add_u64 v[4:5], v[2:3], 0, 16
	s_mov_b64 s[44:45], 0
	global_load_dwordx4 v[30:33], v[2:3], off
	global_load_dwordx4 v[22:25], v[4:5], off
	v_lshl_add_u64 v[4:5], v[2:3], 0, s[12:13]
	global_load_dwordx4 v[26:29], v[4:5], off
	v_lshl_add_u64 v[2:3], v[2:3], 0, s[14:15]
	global_load_dwordx4 v[18:21], v[2:3], off
	s_branch .LBB0_1434

.LBB0_1547:
	ds_read_b128 v[10:13], v183
	ds_read_b128 v[14:17], v183 offset:1024
	ds_read_b128 v[174:177], v183 offset:2048
	ds_read_b128 v[178:181], v183 offset:3072
	s_add_u32 s46, s44, 0xfffc0080
	s_addc_u32 s47, s45, -1
	s_cmp_eq_u32 s80, 12
	s_cselect_b32 s49, s27, s47
	s_cselect_b32 s48, s31, s46
	s_cselect_b32 s47, s25, s79
	s_cselect_b32 s46, s39, s78
	s_mov_b32 m0, s68
	v_lshl_add_u64 v[2:3], s[44:45], 0, v[170:171]
	ds_read_b128 v[188:191], v184
	ds_read_b128 v[192:195], v184 offset:1024
	ds_read_b128 v[196:199], v184 offset:2048
	ds_read_b128 v[200:203], v184 offset:3072
	ds_read_b128 v[204:207], v184 offset:4096
	ds_read_b128 v[208:211], v184 offset:5120
	ds_read_b128 v[212:215], v184 offset:6144
	ds_read_b128 v[216:219], v184 offset:7168
	global_load_lds_dwordx4 v[2:3], off
	v_lshl_add_u64 v[2:3], s[44:45], 0, v[172:173]
	s_mov_b32 m0, s69
	s_nop 0
	global_load_lds_dwordx4 v[2:3], off
	ds_read_b128 v[220:223], v185
	ds_read_b128 v[224:227], v185 offset:1024
	ds_read_b128 v[228:231], v185 offset:2048
	ds_read_b128 v[232:235], v185 offset:3072
	s_waitcnt vmcnt(8) lgkmcnt(0)
	s_barrier
	s_setprio 1
	v_mfma_f32_16x16x128_f8f6f4 v[150:153], v[10:17], v[188:195], v[150:153]
	v_mfma_f32_16x16x128_f8f6f4 v[146:149], v[174:181], v[188:195], v[146:149]
	v_mfma_f32_16x16x128_f8f6f4 v[134:137], v[10:17], v[196:203], v[134:137]
	v_mfma_f32_16x16x128_f8f6f4 v[130:133], v[174:181], v[196:203], v[130:133]
	v_mfma_f32_16x16x128_f8f6f4 v[118:121], v[10:17], v[204:211], v[118:121]
	v_mfma_f32_16x16x128_f8f6f4 v[114:117], v[174:181], v[204:211], v[114:117]
	v_mfma_f32_16x16x128_f8f6f4 v[86:89], v[10:17], v[212:219], v[86:89]
	v_mfma_f32_16x16x128_f8f6f4 v[82:85], v[174:181], v[212:219], v[82:85]
	v_mfma_f32_16x16x128_f8f6f4 v[158:161], v[220:227], v[188:195], v[158:161]
	v_mfma_f32_16x16x128_f8f6f4 v[154:157], v[228:235], v[188:195], v[154:157]
	v_mfma_f32_16x16x128_f8f6f4 v[142:145], v[220:227], v[196:203], v[142:145]
	v_mfma_f32_16x16x128_f8f6f4 v[138:141], v[228:235], v[196:203], v[138:141]
	v_mfma_f32_16x16x128_f8f6f4 v[126:129], v[220:227], v[204:211], v[126:129]
	v_mfma_f32_16x16x128_f8f6f4 v[122:125], v[228:235], v[204:211], v[122:125]
	v_mfma_f32_16x16x128_f8f6f4 v[94:97], v[220:227], v[212:219], v[94:97]
	v_mfma_f32_16x16x128_f8f6f4 v[90:93], v[228:235], v[212:219], v[90:93]
	s_setprio 0
	s_barrier
	ds_read_b128 v[188:191], v184 offset:16384
	ds_read_b128 v[192:195], v184 offset:17408
	ds_read_b128 v[196:199], v184 offset:18432
	ds_read_b128 v[200:203], v184 offset:19456
	ds_read_b128 v[204:207], v184 offset:20480
	ds_read_b128 v[208:211], v184 offset:21504
	ds_read_b128 v[212:215], v184 offset:22528
	ds_read_b128 v[216:219], v184 offset:23552
	s_mov_b32 m0, s70
	v_lshl_add_u64 v[6:7], s[46:47], 0, v[164:165]
	global_load_lds_dwordx4 v[6:7], off
	v_lshl_add_u64 v[8:9], s[46:47], 0, v[168:169]
	s_mov_b32 m0, s71
	s_nop 0
	global_load_lds_dwordx4 v[8:9], off
	s_mov_b32 m0, s54
	v_lshl_add_u64 v[2:3], s[48:49], 0, v[162:163]
	global_load_lds_dwordx4 v[2:3], off
	v_lshl_add_u64 v[4:5], s[48:49], 0, v[166:167]
	s_mov_b32 m0, s55
	s_nop 0
	global_load_lds_dwordx4 v[4:5], off
	s_add_u32 s82, s46, 0x40000
	s_addc_u32 s83, s47, 0
	s_mov_b32 m0, s72
	v_lshl_add_u64 v[236:237], s[82:83], 0, v[164:165]
	global_load_lds_dwordx4 v[236:237], off
	v_lshl_add_u64 v[236:237], s[82:83], 0, v[168:169]
	s_mov_b32 m0, s73
	s_nop 0
	global_load_lds_dwordx4 v[236:237], off
	s_waitcnt vmcnt(8) lgkmcnt(0)
	s_barrier
	s_setprio 1
	v_mfma_f32_16x16x128_f8f6f4 v[110:113], v[10:17], v[188:195], v[110:113]
	v_mfma_f32_16x16x128_f8f6f4 v[102:105], v[174:181], v[188:195], v[102:105]
	v_mfma_f32_16x16x128_f8f6f4 v[78:81], v[10:17], v[196:203], v[78:81]
	v_mfma_f32_16x16x128_f8f6f4 v[70:73], v[174:181], v[196:203], v[70:73]
	v_mfma_f32_16x16x128_f8f6f4 v[62:65], v[10:17], v[204:211], v[62:65]
	v_mfma_f32_16x16x128_f8f6f4 v[54:57], v[174:181], v[204:211], v[54:57]
	v_mfma_f32_16x16x128_f8f6f4 v[46:49], v[10:17], v[212:219], v[46:49]
	v_mfma_f32_16x16x128_f8f6f4 v[42:45], v[174:181], v[212:219], v[42:45]
	v_mfma_f32_16x16x128_f8f6f4 v[106:109], v[220:227], v[188:195], v[106:109]
	v_mfma_f32_16x16x128_f8f6f4 v[98:101], v[228:235], v[188:195], v[98:101]
	v_mfma_f32_16x16x128_f8f6f4 v[74:77], v[220:227], v[196:203], v[74:77]
	v_mfma_f32_16x16x128_f8f6f4 v[66:69], v[228:235], v[196:203], v[66:69]
	v_mfma_f32_16x16x128_f8f6f4 v[58:61], v[220:227], v[204:211], v[58:61]
	v_mfma_f32_16x16x128_f8f6f4 v[50:53], v[228:235], v[204:211], v[50:53]
	v_mfma_f32_16x16x128_f8f6f4 v[38:41], v[220:227], v[212:219], v[38:41]
	v_mfma_f32_16x16x128_f8f6f4 v[34:37], v[228:235], v[212:219], v[34:37]
	s_setprio 0
	s_barrier
	ds_read_b128 v[10:13], v186
	ds_read_b128 v[14:17], v186 offset:1024
	ds_read_b128 v[174:177], v186 offset:2048
	ds_read_b128 v[178:181], v186 offset:3072
	s_add_u32 s48, s48, 0x40000
	s_addc_u32 s49, s49, 0
	s_mov_b32 m0, s56
	v_lshl_add_u64 v[220:221], s[48:49], 0, v[162:163]
	ds_read_b128 v[188:191], v184 offset:32768
	ds_read_b128 v[192:195], v184 offset:33792
	ds_read_b128 v[196:199], v184 offset:34816
	ds_read_b128 v[200:203], v184 offset:35840
	ds_read_b128 v[204:207], v184 offset:36864
	ds_read_b128 v[208:211], v184 offset:37888
	ds_read_b128 v[212:215], v184 offset:38912
	ds_read_b128 v[216:219], v184 offset:39936
	global_load_lds_dwordx4 v[220:221], off
	v_lshl_add_u64 v[220:221], s[48:49], 0, v[166:167]
	s_mov_b32 m0, s57
	s_nop 0
	global_load_lds_dwordx4 v[220:221], off
	ds_read_b128 v[220:223], v187
	ds_read_b128 v[224:227], v187 offset:1024
	ds_read_b128 v[228:231], v187 offset:2048
	ds_read_b128 v[232:235], v187 offset:3072
	s_waitcnt vmcnt(8) lgkmcnt(0)
	s_barrier
	s_setprio 1
	v_mfma_f32_16x16x128_f8f6f4 v[150:153], v[10:17], v[188:195], v[150:153]
	v_mfma_f32_16x16x128_f8f6f4 v[146:149], v[174:181], v[188:195], v[146:149]
	v_mfma_f32_16x16x128_f8f6f4 v[134:137], v[10:17], v[196:203], v[134:137]
	v_mfma_f32_16x16x128_f8f6f4 v[130:133], v[174:181], v[196:203], v[130:133]
	v_mfma_f32_16x16x128_f8f6f4 v[118:121], v[10:17], v[204:211], v[118:121]
	v_mfma_f32_16x16x128_f8f6f4 v[114:117], v[174:181], v[204:211], v[114:117]
	v_mfma_f32_16x16x128_f8f6f4 v[86:89], v[10:17], v[212:219], v[86:89]
	v_mfma_f32_16x16x128_f8f6f4 v[82:85], v[174:181], v[212:219], v[82:85]
	v_mfma_f32_16x16x128_f8f6f4 v[158:161], v[220:227], v[188:195], v[158:161]
	v_mfma_f32_16x16x128_f8f6f4 v[154:157], v[228:235], v[188:195], v[154:157]
	v_mfma_f32_16x16x128_f8f6f4 v[142:145], v[220:227], v[196:203], v[142:145]
	v_mfma_f32_16x16x128_f8f6f4 v[138:141], v[228:235], v[196:203], v[138:141]
	v_mfma_f32_16x16x128_f8f6f4 v[126:129], v[220:227], v[204:211], v[126:129]
	v_mfma_f32_16x16x128_f8f6f4 v[122:125], v[228:235], v[204:211], v[122:125]
	v_mfma_f32_16x16x128_f8f6f4 v[94:97], v[220:227], v[212:219], v[94:97]
	v_mfma_f32_16x16x128_f8f6f4 v[90:93], v[228:235], v[212:219], v[90:93]
	s_setprio 0
	s_barrier
	ds_read_b128 v[188:191], v184 offset:49152
	ds_read_b128 v[192:195], v184 offset:50176
	ds_read_b128 v[196:199], v184 offset:51200
	ds_read_b128 v[200:203], v184 offset:52224
	ds_read_b128 v[204:207], v184 offset:53248
	ds_read_b128 v[208:211], v184 offset:54272
	ds_read_b128 v[212:215], v184 offset:55296
	ds_read_b128 v[216:219], v184 offset:56320
	s_mov_b32 m0, s74
	v_lshl_add_u64 v[6:7], v[6:7], 0, s[10:11]
	global_load_lds_dwordx4 v[6:7], off
	v_lshl_add_u64 v[6:7], v[8:9], 0, s[10:11]
	s_mov_b32 m0, s75
	s_nop 0
	global_load_lds_dwordx4 v[6:7], off
	s_mov_b32 m0, s59
	v_lshl_add_u64 v[2:3], v[2:3], 0, s[10:11]
	global_load_lds_dwordx4 v[2:3], off
	v_lshl_add_u64 v[2:3], v[4:5], 0, s[10:11]
	s_mov_b32 m0, s60
	s_nop 0
	global_load_lds_dwordx4 v[2:3], off
	s_add_u32 s46, s46, 0x40080
	s_addc_u32 s47, s47, 0
	s_mov_b32 m0, s76
	v_lshl_add_u64 v[2:3], s[46:47], 0, v[164:165]
	global_load_lds_dwordx4 v[2:3], off
	v_lshl_add_u64 v[2:3], s[46:47], 0, v[168:169]
	s_mov_b32 m0, s77
	s_nop 0
	global_load_lds_dwordx4 v[2:3], off
	s_waitcnt vmcnt(8) lgkmcnt(0)
	s_barrier
	s_setprio 1
	v_mfma_f32_16x16x128_f8f6f4 v[110:113], v[10:17], v[188:195], v[110:113]
	v_mfma_f32_16x16x128_f8f6f4 v[102:105], v[174:181], v[188:195], v[102:105]
	v_mfma_f32_16x16x128_f8f6f4 v[78:81], v[10:17], v[196:203], v[78:81]
	v_mfma_f32_16x16x128_f8f6f4 v[70:73], v[174:181], v[196:203], v[70:73]
	v_mfma_f32_16x16x128_f8f6f4 v[62:65], v[10:17], v[204:211], v[62:65]
	v_mfma_f32_16x16x128_f8f6f4 v[54:57], v[174:181], v[204:211], v[54:57]
	v_mfma_f32_16x16x128_f8f6f4 v[46:49], v[10:17], v[212:219], v[46:49]
	v_mfma_f32_16x16x128_f8f6f4 v[42:45], v[174:181], v[212:219], v[42:45]
	v_mfma_f32_16x16x128_f8f6f4 v[106:109], v[220:227], v[188:195], v[106:109]
	v_mfma_f32_16x16x128_f8f6f4 v[98:101], v[228:235], v[188:195], v[98:101]
	v_mfma_f32_16x16x128_f8f6f4 v[74:77], v[220:227], v[196:203], v[74:77]
	v_mfma_f32_16x16x128_f8f6f4 v[66:69], v[228:235], v[196:203], v[66:69]
	v_mfma_f32_16x16x128_f8f6f4 v[58:61], v[220:227], v[204:211], v[58:61]
	v_mfma_f32_16x16x128_f8f6f4 v[50:53], v[228:235], v[204:211], v[50:53]
	v_mfma_f32_16x16x128_f8f6f4 v[38:41], v[220:227], v[212:219], v[38:41]
	v_mfma_f32_16x16x128_f8f6f4 v[34:37], v[228:235], v[212:219], v[34:37]
	s_setprio 0
	s_add_i32 s80, s80, 2
	s_add_u32 s44, s44, 0x100
	s_addc_u32 s45, s45, 0
	s_add_u32 s78, s78, 0x100
	s_addc_u32 s79, s79, 0
	s_cmp_gt_u32 s80, 13
	s_barrier
	s_cbranch_scc0 .LBB0_1547
	v_readfirstlane_b32 s99, v0
	s_cmpk_gt_u32 s99, 0xff
	s_cbranch_scc1 .Lz0_1547
	s_barrier
.Lz0_1547:
	v_mov_b32_e32 v2, v0
	s_nop 15
	s_nop 15
	s_lshl_b32 s27, s40, 8
	v_readfirstlane_b32 s25, v2
	s_ashr_i32 s31, s25, 2
	s_andn2_b32 s31, s31, 63
	s_add_i32 s31, s31, s27
	s_lshr_b32 s25, s25, 1
	v_and_or_b32 v10, v2, 15, s31
	s_and_b32 s25, s25, 0x60
	v_lshrrev_b32_e32 v2, 1, v2
	s_lshl_b32 s27, s38, 8
	v_and_b32_e32 v4, 24, v2
	s_or_b32 s27, s25, s27
	v_or_b32_e32 v2, s27, v4
	v_ashrrev_i32_e32 v11, 31, v10
	v_ashrrev_i32_e32 v3, 31, v2
	v_lshlrev_b64 v[6:7], 12, v[10:11]
	v_lshl_add_u64 v[6:7], s[8:9], 0, v[6:7]
	v_lshlrev_b64 v[12:13], 1, v[2:3]
	s_waitcnt vmcnt(6)
	v_lshl_add_u64 v[2:3], v[6:7], 0, v[12:13]
	v_pk_fma_f32 v[6:7], v[150:151], s[18:19], v[22:23] op_sel_hi:[1,0,1]
	v_pk_fma_f32 v[8:9], v[152:153], s[18:19], v[24:25] op_sel_hi:[1,0,1]
	v_cvt_pk_bf16_f32 v6, v6, v7
	v_pk_fma_f32 v[14:15], v[148:149], s[18:19], v[20:21] op_sel_hi:[1,0,1]
	v_cvt_pk_bf16_f32 v7, v8, v9
	v_pk_fma_f32 v[16:17], v[146:147], s[18:19], v[18:19] op_sel_hi:[1,0,1]
	v_pk_fma_f32 v[130:131], v[130:131], s[18:19], v[18:19] op_sel_hi:[1,0,1]
	v_cvt_pk_bf16_f32 v8, v16, v17
	v_cvt_pk_bf16_f32 v9, v14, v15
	global_store_dwordx4 v[2:3], v[6:9], off
	v_pk_fma_f32 v[14:15], v[156:157], s[18:19], v[28:29] op_sel_hi:[1,0,1]
	v_pk_fma_f32 v[16:17], v[154:155], s[18:19], v[26:27] op_sel_hi:[1,0,1]
	v_pk_fma_f32 v[6:7], v[158:159], s[18:19], v[30:31] op_sel_hi:[1,0,1]
	v_pk_fma_f32 v[8:9], v[160:161], s[18:19], v[32:33] op_sel_hi:[1,0,1]
	v_cvt_pk_bf16_f32 v6, v6, v7
	v_pk_fma_f32 v[114:115], v[114:115], s[18:19], v[18:19] op_sel_hi:[1,0,1]
	v_cvt_pk_bf16_f32 v7, v8, v9
	v_cvt_pk_bf16_f32 v8, v16, v17
	v_cvt_pk_bf16_f32 v9, v14, v15
	global_store_dwordx4 v[2:3], v[6:9], off offset:256
	v_pk_fma_f32 v[16:17], v[132:133], s[18:19], v[20:21] op_sel_hi:[1,0,1]
	s_mov_b32 s27, 0x80000
	v_or_b32_e32 v6, 16, v10
	v_ashrrev_i32_e32 v7, 31, v6
	v_lshlrev_b64 v[6:7], 12, v[6:7]
	v_lshl_add_u64 v[6:7], s[8:9], 0, v[6:7]
	v_lshl_add_u64 v[14:15], v[6:7], 0, v[12:13]
	v_pk_fma_f32 v[6:7], v[134:135], s[18:19], v[22:23] op_sel_hi:[1,0,1]
	v_pk_fma_f32 v[8:9], v[136:137], s[18:19], v[24:25] op_sel_hi:[1,0,1]
	v_cvt_pk_bf16_f32 v6, v6, v7
	s_mov_b64 s[38:39], 0x80000
	v_cvt_pk_bf16_f32 v7, v8, v9
	v_cvt_pk_bf16_f32 v8, v130, v131
	v_cvt_pk_bf16_f32 v9, v16, v17
	global_store_dwordx4 v[14:15], v[6:9], off
	v_pk_fma_f32 v[16:17], v[140:141], s[18:19], v[28:29] op_sel_hi:[1,0,1]
	v_pk_fma_f32 v[130:131], v[138:139], s[18:19], v[26:27] op_sel_hi:[1,0,1]
	v_pk_fma_f32 v[6:7], v[142:143], s[18:19], v[30:31] op_sel_hi:[1,0,1]
	v_pk_fma_f32 v[8:9], v[144:145], s[18:19], v[32:33] op_sel_hi:[1,0,1]
	v_cvt_pk_bf16_f32 v6, v6, v7
	v_readlane_b32 s68, v254, 0
	v_cvt_pk_bf16_f32 v7, v8, v9
	v_cvt_pk_bf16_f32 v8, v130, v131
	v_cvt_pk_bf16_f32 v9, v16, v17
	global_store_dwordx4 v[14:15], v[6:9], off offset:256
	v_pk_fma_f32 v[16:17], v[116:117], s[18:19], v[20:21] op_sel_hi:[1,0,1]
	v_readlane_b32 s69, v254, 1
	v_or_b32_e32 v6, 32, v10
	v_ashrrev_i32_e32 v7, 31, v6
	v_lshlrev_b64 v[6:7], 12, v[6:7]
	v_lshl_add_u64 v[6:7], s[8:9], 0, v[6:7]
	v_lshl_add_u64 v[14:15], v[6:7], 0, v[12:13]
	v_pk_fma_f32 v[6:7], v[118:119], s[18:19], v[22:23] op_sel_hi:[1,0,1]
	v_pk_fma_f32 v[8:9], v[120:121], s[18:19], v[24:25] op_sel_hi:[1,0,1]
	v_cvt_pk_bf16_f32 v6, v6, v7
	v_readlane_b32 s70, v254, 2
	v_cvt_pk_bf16_f32 v7, v8, v9
	v_cvt_pk_bf16_f32 v8, v114, v115
	v_cvt_pk_bf16_f32 v9, v16, v17
	global_store_dwordx4 v[14:15], v[6:9], off
	v_pk_fma_f32 v[16:17], v[124:125], s[18:19], v[28:29] op_sel_hi:[1,0,1]
	v_pk_fma_f32 v[114:115], v[122:123], s[18:19], v[26:27] op_sel_hi:[1,0,1]
	v_pk_fma_f32 v[6:7], v[126:127], s[18:19], v[30:31] op_sel_hi:[1,0,1]
	v_pk_fma_f32 v[8:9], v[128:129], s[18:19], v[32:33] op_sel_hi:[1,0,1]
	v_cvt_pk_bf16_f32 v6, v6, v7
	v_readlane_b32 s71, v254, 3
	v_cvt_pk_bf16_f32 v7, v8, v9
	v_cvt_pk_bf16_f32 v8, v114, v115
	v_cvt_pk_bf16_f32 v9, v16, v17
	global_store_dwordx4 v[14:15], v[6:9], off offset:256
	v_pk_fma_f32 v[14:15], v[82:83], s[18:19], v[18:19] op_sel_hi:[1,0,1]
	v_readlane_b32 s72, v254, 4
	v_or_b32_e32 v6, 48, v10
	v_ashrrev_i32_e32 v7, 31, v6
	v_lshlrev_b64 v[6:7], 12, v[6:7]
	v_lshl_add_u64 v[6:7], s[8:9], 0, v[6:7]
	v_lshl_add_u64 v[10:11], v[6:7], 0, v[12:13]
	v_pk_fma_f32 v[8:9], v[88:89], s[18:19], v[24:25] op_sel_hi:[1,0,1]
	v_pk_fma_f32 v[6:7], v[86:87], s[18:19], v[22:23] op_sel_hi:[1,0,1]
	v_pk_fma_f32 v[12:13], v[84:85], s[18:19], v[20:21] op_sel_hi:[1,0,1]
	v_cvt_pk_bf16_f32 v6, v6, v7
	v_cvt_pk_bf16_f32 v7, v8, v9
	v_cvt_pk_bf16_f32 v8, v14, v15
	v_pk_fma_f32 v[14:15], v[90:91], s[18:19], v[26:27] op_sel_hi:[1,0,1]
	v_cvt_pk_bf16_f32 v9, v12, v13
	global_store_dwordx4 v[10:11], v[6:9], off
	v_pk_fma_f32 v[12:13], v[92:93], s[18:19], v[28:29] op_sel_hi:[1,0,1]
	v_readlane_b32 s73, v254, 5
	v_pk_fma_f32 v[8:9], v[96:97], s[18:19], v[32:33] op_sel_hi:[1,0,1]
	v_pk_fma_f32 v[6:7], v[94:95], s[18:19], v[30:31] op_sel_hi:[1,0,1]
	v_readlane_b32 s74, v254, 6
	v_cvt_pk_bf16_f32 v6, v6, v7
	v_cvt_pk_bf16_f32 v7, v8, v9
	v_cvt_pk_bf16_f32 v8, v14, v15
	v_cvt_pk_bf16_f32 v9, v12, v13
	global_store_dwordx4 v[10:11], v[6:9], off offset:256
	v_pk_fma_f32 v[12:13], v[104:105], s[18:19], v[20:21] op_sel_hi:[1,0,1]
	v_pk_fma_f32 v[14:15], v[102:103], s[18:19], v[18:19] op_sel_hi:[1,0,1]
	v_pk_fma_f32 v[8:9], v[112:113], s[18:19], v[24:25] op_sel_hi:[1,0,1]
	v_pk_fma_f32 v[6:7], v[110:111], s[18:19], v[22:23] op_sel_hi:[1,0,1]
	v_lshl_add_u64 v[10:11], v[2:3], 0, s[38:39]
	v_cvt_pk_bf16_f32 v6, v6, v7
	v_cvt_pk_bf16_f32 v7, v8, v9
	v_cvt_pk_bf16_f32 v8, v14, v15
	v_cvt_pk_bf16_f32 v9, v12, v13
	v_add_co_u32_e32 v12, vcc, s27, v2
	v_pk_fma_f32 v[14:15], v[98:99], s[18:19], v[26:27] op_sel_hi:[1,0,1]
	s_nop 0
	v_addc_co_u32_e32 v13, vcc, 0, v3, vcc
	global_store_dwordx4 v[12:13], v[6:9], off
	v_pk_fma_f32 v[12:13], v[100:101], s[18:19], v[28:29] op_sel_hi:[1,0,1]
	s_mov_b32 s27, 0x90000
	v_pk_fma_f32 v[8:9], v[108:109], s[18:19], v[32:33] op_sel_hi:[1,0,1]
	v_pk_fma_f32 v[6:7], v[106:107], s[18:19], v[30:31] op_sel_hi:[1,0,1]
	s_mov_b64 s[38:39], 0x90000
	v_cvt_pk_bf16_f32 v6, v6, v7
	v_cvt_pk_bf16_f32 v7, v8, v9
	v_cvt_pk_bf16_f32 v8, v14, v15
	v_cvt_pk_bf16_f32 v9, v12, v13
	global_store_dwordx4 v[10:11], v[6:9], off offset:256
	v_pk_fma_f32 v[12:13], v[72:73], s[18:19], v[20:21] op_sel_hi:[1,0,1]
	v_pk_fma_f32 v[14:15], v[70:71], s[18:19], v[18:19] op_sel_hi:[1,0,1]
	v_pk_fma_f32 v[8:9], v[80:81], s[18:19], v[24:25] op_sel_hi:[1,0,1]
	v_pk_fma_f32 v[6:7], v[78:79], s[18:19], v[22:23] op_sel_hi:[1,0,1]
	v_lshl_add_u64 v[10:11], v[2:3], 0, s[38:39]
	v_cvt_pk_bf16_f32 v6, v6, v7
	v_cvt_pk_bf16_f32 v7, v8, v9
	v_cvt_pk_bf16_f32 v8, v14, v15
	v_cvt_pk_bf16_f32 v9, v12, v13
	v_add_co_u32_e32 v12, vcc, s27, v2
	v_pk_fma_f32 v[14:15], v[66:67], s[18:19], v[26:27] op_sel_hi:[1,0,1]
	s_nop 0
	v_addc_co_u32_e32 v13, vcc, 0, v3, vcc
	global_store_dwordx4 v[12:13], v[6:9], off
	v_pk_fma_f32 v[12:13], v[68:69], s[18:19], v[28:29] op_sel_hi:[1,0,1]
	s_mov_b64 s[38:39], 0xa0000
	v_pk_fma_f32 v[8:9], v[76:77], s[18:19], v[32:33] op_sel_hi:[1,0,1]
	v_pk_fma_f32 v[6:7], v[74:75], s[18:19], v[30:31] op_sel_hi:[1,0,1]
	v_readlane_b32 s75, v254, 7
	v_cvt_pk_bf16_f32 v6, v6, v7
	v_cvt_pk_bf16_f32 v7, v8, v9
	v_cvt_pk_bf16_f32 v8, v14, v15
	v_cvt_pk_bf16_f32 v9, v12, v13
	global_store_dwordx4 v[10:11], v[6:9], off offset:256
	v_pk_fma_f32 v[12:13], v[56:57], s[18:19], v[20:21] op_sel_hi:[1,0,1]
	v_pk_fma_f32 v[14:15], v[54:55], s[18:19], v[18:19] op_sel_hi:[1,0,1]
	v_pk_fma_f32 v[8:9], v[64:65], s[18:19], v[24:25] op_sel_hi:[1,0,1]
	v_pk_fma_f32 v[6:7], v[62:63], s[18:19], v[22:23] op_sel_hi:[1,0,1]
	v_lshl_add_u64 v[10:11], v[2:3], 0, s[38:39]
	v_cvt_pk_bf16_f32 v6, v6, v7
	v_cvt_pk_bf16_f32 v7, v8, v9
	v_cvt_pk_bf16_f32 v8, v14, v15
	v_cvt_pk_bf16_f32 v9, v12, v13
	v_add_co_u32_e32 v12, vcc, s66, v2
	v_pk_fma_f32 v[14:15], v[50:51], s[18:19], v[26:27] op_sel_hi:[1,0,1]
	s_nop 0
	v_addc_co_u32_e32 v13, vcc, 0, v3, vcc
	global_store_dwordx4 v[12:13], v[6:9], off
	v_pk_fma_f32 v[12:13], v[52:53], s[18:19], v[28:29] op_sel_hi:[1,0,1]
	s_mov_b64 s[38:39], -1
	v_pk_fma_f32 v[8:9], v[60:61], s[18:19], v[32:33] op_sel_hi:[1,0,1]
	v_pk_fma_f32 v[6:7], v[58:59], s[18:19], v[30:31] op_sel_hi:[1,0,1]
	s_nop 0
	v_cvt_pk_bf16_f32 v6, v6, v7
	v_cvt_pk_bf16_f32 v7, v8, v9
	v_cvt_pk_bf16_f32 v8, v14, v15
	v_cvt_pk_bf16_f32 v9, v12, v13
	global_store_dwordx4 v[10:11], v[6:9], off offset:256
	v_lshl_add_u64 v[10:11], v[2:3], 0, s[20:21]
	v_add_co_u32_e32 v2, vcc, s67, v2
	v_pk_fma_f32 v[8:9], v[48:49], s[18:19], v[24:25] op_sel_hi:[1,0,1]
	v_pk_fma_f32 v[6:7], v[46:47], s[18:19], v[22:23] op_sel_hi:[1,0,1]
	v_pk_fma_f32 v[12:13], v[44:45], s[18:19], v[20:21] op_sel_hi:[1,0,1]
	v_pk_fma_f32 v[14:15], v[42:43], s[18:19], v[18:19] op_sel_hi:[1,0,1]
	v_cvt_pk_bf16_f32 v6, v6, v7
	v_cvt_pk_bf16_f32 v7, v8, v9
	v_addc_co_u32_e32 v3, vcc, 0, v3, vcc
	v_cvt_pk_bf16_f32 v8, v14, v15
	v_cvt_pk_bf16_f32 v9, v12, v13
	global_store_dwordx4 v[2:3], v[6:9], off
	s_and_b64 vcc, s[42:43], exec
	v_pk_fma_f32 v[2:3], v[40:41], s[18:19], v[32:33] op_sel_hi:[1,0,1]
	v_pk_fma_f32 v[6:7], v[38:39], s[18:19], v[30:31] op_sel_hi:[1,0,1]
	v_pk_fma_f32 v[8:9], v[34:35], s[18:19], v[26:27] op_sel_hi:[1,0,1]
	v_pk_fma_f32 v[12:13], v[36:37], s[18:19], v[28:29] op_sel_hi:[1,0,1]
	v_cvt_pk_bf16_f32 v6, v6, v7
	v_cvt_pk_bf16_f32 v7, v2, v3
	v_cvt_pk_bf16_f32 v8, v8, v9
	s_nop 0
	v_cvt_pk_bf16_f32 v9, v12, v13
	global_store_dwordx4 v[10:11], v[6:9], off offset:256
	v_readfirstlane_b32 s99, v0
	s_cmpk_gt_u32 s99, 0xff
	s_cbranch_scc0 .Lz1_1547
	s_barrier
.Lz1_1547:
	s_cbranch_vccz .LBB0_1541
	s_lshl_b32 s27, s24, 8
	s_or_b32 s25, s25, s27
	v_or_b32_e32 v2, s25, v4
	v_ashrrev_i32_e32 v3, 31, v2
	v_mov_b32_e32 v18, 0
	s_and_b64 vcc, exec, s[6:7]
	v_mov_b32_e32 v22, 0
	v_mov_b32_e32 v23, 0
	v_mov_b32_e32 v24, 0
	v_mov_b32_e32 v25, 0
	s_cbranch_vccnz .LBB0_1551
	s_ashr_i32 s27, s26, 31
	s_lshl_b64 s[38:39], s[26:27], 13
	s_add_u32 s38, s68, s38
	s_addc_u32 s39, s69, s39
	v_lshl_add_u64 v[4:5], v[2:3], 2, s[38:39]
	global_load_dwordx4 v[22:25], v[4:5], off
